# combine phase hand-rewritten (fully unrolled 16 rows, counted waits, hoisted gains, lane-contiguous rows); on top of gating + topk rewrites
# baseline (speedup 1.0000x reference)
.LBB0_1424:
.Lcb_new:
	s_cmp_lg_u32 s96, 0x100
	s_cbranch_scc1 .Lcb_old
	v_readlane_b32 s12, v253, 0
	v_readlane_b32 s13, v253, 1
	s_nop 0
	s_load_dwordx2 s[0:1], s[12:13], 0xa0
	s_load_dwordx2 s[14:15], s[12:13], 0x98
	s_load_dwordx2 s[16:17], s[12:13], 0x8
	v_and_b32_e32 v205, 63, v0
	v_lshrrev_b32_e32 v204, 6, v0
	v_lshlrev_b32_e32 v212, 4, v205
	v_lshlrev_b32_e32 v213, 5, v205
	v_lshlrev_b32_e32 v214, 6, v205
	v_readfirstlane_b32 s8, v204
	v_and_b32_e32 v215, 15, v205
	v_lshlrev_b32_e32 v215, 14, v215
	s_add_i32 s8, s8, s89
	s_mov_b32 s6, 0x3d000000
	s_mov_b32 s7, 0x3d000000
	s_waitcnt lgkmcnt(0)
	s_add_u32 s4, s0, 0x57e00000
	s_addc_u32 s5, s1, 0
	s_min_u32 s10, s52, 2
	s_add_i32 s10, s10, 1
	s_lshl_b32 s10, s10, 12
	s_add_u32 s16, s16, s10
	s_addc_u32 s17, s17, 0
	global_load_dwordx4 v[2:5], v214, s[16:17]
	global_load_dwordx4 v[6:9], v214, s[16:17] offset:16
	global_load_dwordx4 v[10:13], v214, s[16:17] offset:32
	global_load_dwordx4 v[14:17], v214, s[16:17] offset:48
	s_mov_b32 s9, s8
	s_lshr_b32 s10, s9, 12
	s_lshl_b32 s10, s10, 18
	s_and_b32 s12, s9, 0xfff
	s_lshl_b32 s12, s12, 2
	s_add_i32 s10, s10, s12
	s_add_u32 s12, s0, 0x37b00000
	s_addc_u32 s13, s1, 0
	s_add_u32 s12, s12, s10
	s_addc_u32 s13, s13, 0
	global_load_dword v66, v215, s[12:13]
	s_lshl_b32 s10, s9, 11
	s_add_u32 s12, s0, 0x37e00000
	s_addc_u32 s13, s1, 0
	s_add_u32 s12, s12, s10
	s_addc_u32 s13, s13, 0
	global_load_dwordx4 v[18:21], v213, s[12:13] nt
	global_load_dwordx4 v[22:25], v213, s[12:13] offset:16 nt
	s_add_i32 s9, s8, 0x800
	s_lshr_b32 s10, s9, 12
	s_lshl_b32 s10, s10, 18
	s_and_b32 s12, s9, 0xfff
	s_lshl_b32 s12, s12, 2
	s_add_i32 s10, s10, s12
	s_add_u32 s12, s0, 0x37b00000
	s_addc_u32 s13, s1, 0
	s_add_u32 s12, s12, s10
	s_addc_u32 s13, s13, 0
	global_load_dword v67, v215, s[12:13]
	s_lshl_b32 s10, s9, 11
	s_add_u32 s12, s0, 0x37e00000
	s_addc_u32 s13, s1, 0
	s_add_u32 s12, s12, s10
	s_addc_u32 s13, s13, 0
	global_load_dwordx4 v[26:29], v213, s[12:13] nt
	global_load_dwordx4 v[30:33], v213, s[12:13] offset:16 nt
	s_add_i32 s9, s8, 0x1000
	s_lshr_b32 s10, s9, 12
	s_lshl_b32 s10, s10, 18
	s_and_b32 s12, s9, 0xfff
	s_lshl_b32 s12, s12, 2
	s_add_i32 s10, s10, s12
	s_add_u32 s12, s0, 0x37b00000
	s_addc_u32 s13, s1, 0
	s_add_u32 s12, s12, s10
	s_addc_u32 s13, s13, 0
	global_load_dword v68, v215, s[12:13]
	s_lshl_b32 s10, s9, 11
	s_add_u32 s12, s0, 0x37e00000
	s_addc_u32 s13, s1, 0
	s_add_u32 s12, s12, s10
	s_addc_u32 s13, s13, 0
	global_load_dwordx4 v[34:37], v213, s[12:13] nt
	global_load_dwordx4 v[38:41], v213, s[12:13] offset:16 nt
	s_add_i32 s9, s8, 0x1800
	s_lshr_b32 s10, s9, 12
	s_lshl_b32 s10, s10, 18
	s_and_b32 s12, s9, 0xfff
	s_lshl_b32 s12, s12, 2
	s_add_i32 s10, s10, s12
	s_add_u32 s12, s0, 0x37b00000
	s_addc_u32 s13, s1, 0
	s_add_u32 s12, s12, s10
	s_addc_u32 s13, s13, 0
	global_load_dword v69, v215, s[12:13]
	s_lshl_b32 s10, s9, 11
	s_add_u32 s12, s0, 0x37e00000
	s_addc_u32 s13, s1, 0
	s_add_u32 s12, s12, s10
	s_addc_u32 s13, s13, 0
	global_load_dwordx4 v[42:45], v213, s[12:13] nt
	global_load_dwordx4 v[46:49], v213, s[12:13] offset:16 nt
	s_add_i32 s9, s8, 0x2000
	s_lshr_b32 s10, s9, 12
	s_lshl_b32 s10, s10, 18
	s_and_b32 s12, s9, 0xfff
	s_lshl_b32 s12, s12, 2
	s_add_i32 s10, s10, s12
	s_add_u32 s12, s0, 0x37b00000
	s_addc_u32 s13, s1, 0
	s_add_u32 s12, s12, s10
	s_addc_u32 s13, s13, 0
	global_load_dword v70, v215, s[12:13]
	s_lshl_b32 s10, s9, 11
	s_add_u32 s12, s0, 0x37e00000
	s_addc_u32 s13, s1, 0
	s_add_u32 s12, s12, s10
	s_addc_u32 s13, s13, 0
	global_load_dwordx4 v[50:53], v213, s[12:13] nt
	global_load_dwordx4 v[54:57], v213, s[12:13] offset:16 nt
	s_add_i32 s9, s8, 0x2800
	s_lshr_b32 s10, s9, 12
	s_lshl_b32 s10, s10, 18
	s_and_b32 s12, s9, 0xfff
	s_lshl_b32 s12, s12, 2
	s_add_i32 s10, s10, s12
	s_add_u32 s12, s0, 0x37b00000
	s_addc_u32 s13, s1, 0
	s_add_u32 s12, s12, s10
	s_addc_u32 s13, s13, 0
	global_load_dword v71, v215, s[12:13]
	s_lshl_b32 s10, s9, 11
	s_add_u32 s12, s0, 0x37e00000
	s_addc_u32 s13, s1, 0
	s_add_u32 s12, s12, s10
	s_addc_u32 s13, s13, 0
	global_load_dwordx4 v[58:61], v213, s[12:13] nt
	global_load_dwordx4 v[62:65], v213, s[12:13] offset:16 nt
	s_waitcnt vmcnt(15)
	v_cmp_le_i32_e64 s[24:25], 0, v66
	s_mov_b32 s10, 0
	s_and_b32 s9, s24, 0xffff
	s_cmp_lg_u32 s9, 0
	s_cbranch_scc0 .Lcb_n0_0
	s_ff1_i32_b32 s26, s9
	s_add_i32 s27, s9, -1
	v_readlane_b32 s26, v66, s26
	s_and_b32 s9, s9, s27
	s_bitset1_b32 s10, 0
	s_lshl_b32 s26, s26, 10
	s_add_u32 s26, s4, s26
	s_addc_u32 s27, s5, 0
	s_branch .Lcb_l0_0
.Lcb_n0_0:
	s_mov_b64 s[26:27], s[4:5]
.Lcb_l0_0:
	global_load_dwordx4 v[72:75], v212, s[26:27] nt
	s_cmp_lg_u32 s9, 0
	s_cbranch_scc0 .Lcb_n0_1
	s_ff1_i32_b32 s26, s9
	s_add_i32 s27, s9, -1
	v_readlane_b32 s26, v66, s26
	s_and_b32 s9, s9, s27
	s_bitset1_b32 s10, 1
	s_lshl_b32 s26, s26, 10
	s_add_u32 s26, s4, s26
	s_addc_u32 s27, s5, 0
	s_branch .Lcb_l0_1

.Lcb_l0_1:
	global_load_dwordx4 v[76:79], v212, s[26:27] nt
	s_cmp_lg_u32 s9, 0
	s_cbranch_scc0 .Lcb_n0_2
	s_ff1_i32_b32 s26, s9
	s_add_i32 s27, s9, -1
	v_readlane_b32 s26, v66, s26
	s_and_b32 s9, s9, s27
	s_bitset1_b32 s10, 2
	s_lshl_b32 s26, s26, 10
	s_add_u32 s26, s4, s26
	s_addc_u32 s27, s5, 0
	s_branch .Lcb_l0_2

.Lcb_l0_2:
	global_load_dwordx4 v[80:83], v212, s[26:27] nt
	s_cmp_lg_u32 s9, 0
	s_cbranch_scc0 .Lcb_n0_3
	s_ff1_i32_b32 s26, s9
	s_add_i32 s27, s9, -1
	v_readlane_b32 s26, v66, s26
	s_and_b32 s9, s9, s27
	s_bitset1_b32 s10, 3
	s_lshl_b32 s26, s26, 10
	s_add_u32 s26, s4, s26
	s_addc_u32 s27, s5, 0
	s_branch .Lcb_l0_3

.Lcb_l0_3:
	global_load_dwordx4 v[84:87], v212, s[26:27] nt
	s_cmp_lg_u32 s9, 0
	s_cbranch_scc0 .Lcb_n0_4
	s_ff1_i32_b32 s26, s9
	s_add_i32 s27, s9, -1
	v_readlane_b32 s26, v66, s26
	s_and_b32 s9, s9, s27
	s_bitset1_b32 s10, 4
	s_lshl_b32 s26, s26, 10
	s_add_u32 s26, s4, s26
	s_addc_u32 s27, s5, 0
	s_branch .Lcb_l0_4

.Lcb_l0_4:
	global_load_dwordx4 v[88:91], v212, s[26:27] nt
	s_cmp_lg_u32 s9, 0
	s_cbranch_scc0 .Lcb_n0_5
	s_ff1_i32_b32 s26, s9
	s_add_i32 s27, s9, -1
	v_readlane_b32 s26, v66, s26
	s_and_b32 s9, s9, s27
	s_bitset1_b32 s10, 5
	s_lshl_b32 s26, s26, 10
	s_add_u32 s26, s4, s26
	s_addc_u32 s27, s5, 0
	s_branch .Lcb_l0_5

.Lcb_l0_5:
	global_load_dwordx4 v[92:95], v212, s[26:27] nt
	v_writelane_b32 v210, s10, 0
	v_writelane_b32 v211, s9, 0
	s_waitcnt vmcnt(18)
	v_cmp_le_i32_e64 s[24:25], 0, v67
	s_mov_b32 s10, 0
	s_and_b32 s9, s24, 0xffff
	s_cmp_lg_u32 s9, 0
	s_cbranch_scc0 .Lcb_n1_0
	s_ff1_i32_b32 s26, s9
	s_add_i32 s27, s9, -1
	v_readlane_b32 s26, v67, s26
	s_and_b32 s9, s9, s27
	s_bitset1_b32 s10, 0
	s_lshl_b32 s26, s26, 10
	s_add_u32 s26, s4, s26
	s_addc_u32 s27, s5, 0
	s_branch .Lcb_l1_0

.Lcb_l1_0:
	global_load_dwordx4 v[96:99], v212, s[26:27] nt
	s_cmp_lg_u32 s9, 0
	s_cbranch_scc0 .Lcb_n1_1
	s_ff1_i32_b32 s26, s9
	s_add_i32 s27, s9, -1
	v_readlane_b32 s26, v67, s26
	s_and_b32 s9, s9, s27
	s_bitset1_b32 s10, 1
	s_lshl_b32 s26, s26, 10
	s_add_u32 s26, s4, s26
	s_addc_u32 s27, s5, 0
	s_branch .Lcb_l1_1

.Lcb_l1_1:
	global_load_dwordx4 v[100:103], v212, s[26:27] nt
	s_cmp_lg_u32 s9, 0
	s_cbranch_scc0 .Lcb_n1_2
	s_ff1_i32_b32 s26, s9
	s_add_i32 s27, s9, -1
	v_readlane_b32 s26, v67, s26
	s_and_b32 s9, s9, s27
	s_bitset1_b32 s10, 2
	s_lshl_b32 s26, s26, 10
	s_add_u32 s26, s4, s26
	s_addc_u32 s27, s5, 0
	s_branch .Lcb_l1_2

.Lcb_l1_2:
	global_load_dwordx4 v[104:107], v212, s[26:27] nt
	s_cmp_lg_u32 s9, 0
	s_cbranch_scc0 .Lcb_n1_3
	s_ff1_i32_b32 s26, s9
	s_add_i32 s27, s9, -1
	v_readlane_b32 s26, v67, s26
	s_and_b32 s9, s9, s27
	s_bitset1_b32 s10, 3
	s_lshl_b32 s26, s26, 10
	s_add_u32 s26, s4, s26
	s_addc_u32 s27, s5, 0
	s_branch .Lcb_l1_3

.Lcb_l1_3:
	global_load_dwordx4 v[108:111], v212, s[26:27] nt
	s_cmp_lg_u32 s9, 0
	s_cbranch_scc0 .Lcb_n1_4
	s_ff1_i32_b32 s26, s9
	s_add_i32 s27, s9, -1
	v_readlane_b32 s26, v67, s26
	s_and_b32 s9, s9, s27
	s_bitset1_b32 s10, 4
	s_lshl_b32 s26, s26, 10
	s_add_u32 s26, s4, s26
	s_addc_u32 s27, s5, 0
	s_branch .Lcb_l1_4

.Lcb_l1_4:
	global_load_dwordx4 v[112:115], v212, s[26:27] nt
	s_cmp_lg_u32 s9, 0
	s_cbranch_scc0 .Lcb_n1_5
	s_ff1_i32_b32 s26, s9
	s_add_i32 s27, s9, -1
	v_readlane_b32 s26, v67, s26
	s_and_b32 s9, s9, s27
	s_bitset1_b32 s10, 5
	s_lshl_b32 s26, s26, 10
	s_add_u32 s26, s4, s26
	s_addc_u32 s27, s5, 0
	s_branch .Lcb_l1_5

.Lcb_l1_5:
	global_load_dwordx4 v[116:119], v212, s[26:27] nt
	v_writelane_b32 v210, s10, 1
	v_writelane_b32 v211, s9, 1
	s_waitcnt vmcnt(21)
	v_cmp_le_i32_e64 s[24:25], 0, v68
	s_mov_b32 s10, 0
	s_and_b32 s9, s24, 0xffff
	s_cmp_lg_u32 s9, 0
	s_cbranch_scc0 .Lcb_n2_0
	s_ff1_i32_b32 s26, s9
	s_add_i32 s27, s9, -1
	v_readlane_b32 s26, v68, s26
	s_and_b32 s9, s9, s27
	s_bitset1_b32 s10, 0
	s_lshl_b32 s26, s26, 10
	s_add_u32 s26, s4, s26
	s_addc_u32 s27, s5, 0
	s_branch .Lcb_l2_0

.Lcb_l2_0:
	global_load_dwordx4 v[120:123], v212, s[26:27] nt
	s_cmp_lg_u32 s9, 0
	s_cbranch_scc0 .Lcb_n2_1
	s_ff1_i32_b32 s26, s9
	s_add_i32 s27, s9, -1
	v_readlane_b32 s26, v68, s26
	s_and_b32 s9, s9, s27
	s_bitset1_b32 s10, 1
	s_lshl_b32 s26, s26, 10
	s_add_u32 s26, s4, s26
	s_addc_u32 s27, s5, 0
	s_branch .Lcb_l2_1

.Lcb_l2_1:
	global_load_dwordx4 v[124:127], v212, s[26:27] nt
	s_cmp_lg_u32 s9, 0
	s_cbranch_scc0 .Lcb_n2_2
	s_ff1_i32_b32 s26, s9
	s_add_i32 s27, s9, -1
	v_readlane_b32 s26, v68, s26
	s_and_b32 s9, s9, s27
	s_bitset1_b32 s10, 2
	s_lshl_b32 s26, s26, 10
	s_add_u32 s26, s4, s26
	s_addc_u32 s27, s5, 0
	s_branch .Lcb_l2_2

.Lcb_l2_2:
	global_load_dwordx4 v[128:131], v212, s[26:27] nt
	s_cmp_lg_u32 s9, 0
	s_cbranch_scc0 .Lcb_n2_3
	s_ff1_i32_b32 s26, s9
	s_add_i32 s27, s9, -1
	v_readlane_b32 s26, v68, s26
	s_and_b32 s9, s9, s27
	s_bitset1_b32 s10, 3
	s_lshl_b32 s26, s26, 10
	s_add_u32 s26, s4, s26
	s_addc_u32 s27, s5, 0
	s_branch .Lcb_l2_3

.Lcb_l2_3:
	global_load_dwordx4 v[132:135], v212, s[26:27] nt
	s_cmp_lg_u32 s9, 0
	s_cbranch_scc0 .Lcb_n2_4
	s_ff1_i32_b32 s26, s9
	s_add_i32 s27, s9, -1
	v_readlane_b32 s26, v68, s26
	s_and_b32 s9, s9, s27
	s_bitset1_b32 s10, 4
	s_lshl_b32 s26, s26, 10
	s_add_u32 s26, s4, s26
	s_addc_u32 s27, s5, 0
	s_branch .Lcb_l2_4

.Lcb_l2_4:
	global_load_dwordx4 v[136:139], v212, s[26:27] nt
	s_cmp_lg_u32 s9, 0
	s_cbranch_scc0 .Lcb_n2_5
	s_ff1_i32_b32 s26, s9
	s_add_i32 s27, s9, -1
	v_readlane_b32 s26, v68, s26
	s_and_b32 s9, s9, s27
	s_bitset1_b32 s10, 5
	s_lshl_b32 s26, s26, 10
	s_add_u32 s26, s4, s26
	s_addc_u32 s27, s5, 0
	s_branch .Lcb_l2_5

.Lcb_l2_5:
	global_load_dwordx4 v[140:143], v212, s[26:27] nt
	v_writelane_b32 v210, s10, 2
	v_writelane_b32 v211, s9, 2
	s_waitcnt vmcnt(24)
	v_cmp_le_i32_e64 s[24:25], 0, v69
	s_mov_b32 s10, 0
	s_and_b32 s9, s24, 0xffff
	s_cmp_lg_u32 s9, 0
	s_cbranch_scc0 .Lcb_n3_0
	s_ff1_i32_b32 s26, s9
	s_add_i32 s27, s9, -1
	v_readlane_b32 s26, v69, s26
	s_and_b32 s9, s9, s27
	s_bitset1_b32 s10, 0
	s_lshl_b32 s26, s26, 10
	s_add_u32 s26, s4, s26
	s_addc_u32 s27, s5, 0
	s_branch .Lcb_l3_0

.Lcb_l3_0:
	global_load_dwordx4 v[144:147], v212, s[26:27] nt
	s_cmp_lg_u32 s9, 0
	s_cbranch_scc0 .Lcb_n3_1
	s_ff1_i32_b32 s26, s9
	s_add_i32 s27, s9, -1
	v_readlane_b32 s26, v69, s26
	s_and_b32 s9, s9, s27
	s_bitset1_b32 s10, 1
	s_lshl_b32 s26, s26, 10
	s_add_u32 s26, s4, s26
	s_addc_u32 s27, s5, 0
	s_branch .Lcb_l3_1

.Lcb_l3_1:
	global_load_dwordx4 v[148:151], v212, s[26:27] nt
	s_cmp_lg_u32 s9, 0
	s_cbranch_scc0 .Lcb_n3_2
	s_ff1_i32_b32 s26, s9
	s_add_i32 s27, s9, -1
	v_readlane_b32 s26, v69, s26
	s_and_b32 s9, s9, s27
	s_bitset1_b32 s10, 2
	s_lshl_b32 s26, s26, 10
	s_add_u32 s26, s4, s26
	s_addc_u32 s27, s5, 0
	s_branch .Lcb_l3_2

.Lcb_l3_2:
	global_load_dwordx4 v[152:155], v212, s[26:27] nt
	s_cmp_lg_u32 s9, 0
	s_cbranch_scc0 .Lcb_n3_3
	s_ff1_i32_b32 s26, s9
	s_add_i32 s27, s9, -1
	v_readlane_b32 s26, v69, s26
	s_and_b32 s9, s9, s27
	s_bitset1_b32 s10, 3
	s_lshl_b32 s26, s26, 10
	s_add_u32 s26, s4, s26
	s_addc_u32 s27, s5, 0
	s_branch .Lcb_l3_3

.Lcb_l3_3:
	global_load_dwordx4 v[156:159], v212, s[26:27] nt
	s_cmp_lg_u32 s9, 0
	s_cbranch_scc0 .Lcb_n3_4
	s_ff1_i32_b32 s26, s9
	s_add_i32 s27, s9, -1
	v_readlane_b32 s26, v69, s26
	s_and_b32 s9, s9, s27
	s_bitset1_b32 s10, 4
	s_lshl_b32 s26, s26, 10
	s_add_u32 s26, s4, s26
	s_addc_u32 s27, s5, 0
	s_branch .Lcb_l3_4

.Lcb_l3_4:
	global_load_dwordx4 v[160:163], v212, s[26:27] nt
	s_cmp_lg_u32 s9, 0
	s_cbranch_scc0 .Lcb_n3_5
	s_ff1_i32_b32 s26, s9
	s_add_i32 s27, s9, -1
	v_readlane_b32 s26, v69, s26
	s_and_b32 s9, s9, s27
	s_bitset1_b32 s10, 5
	s_lshl_b32 s26, s26, 10
	s_add_u32 s26, s4, s26
	s_addc_u32 s27, s5, 0
	s_branch .Lcb_l3_5

.Lcb_l3_5:
	global_load_dwordx4 v[164:167], v212, s[26:27] nt
	v_writelane_b32 v210, s10, 3
	v_writelane_b32 v211, s9, 3
	s_waitcnt vmcnt(42)
	s_waitcnt vmcnt(18)
	v_lshlrev_b32_e32 v168, 16, v18
	v_and_b32_e32 v169, 0xffff0000, v18
	v_lshlrev_b32_e32 v170, 16, v19
	v_and_b32_e32 v171, 0xffff0000, v19
	v_lshlrev_b32_e32 v172, 16, v20
	v_and_b32_e32 v173, 0xffff0000, v20
	v_lshlrev_b32_e32 v174, 16, v21
	v_and_b32_e32 v175, 0xffff0000, v21
	v_lshlrev_b32_e32 v176, 16, v22
	v_and_b32_e32 v177, 0xffff0000, v22
	v_lshlrev_b32_e32 v178, 16, v23
	v_and_b32_e32 v179, 0xffff0000, v23
	v_lshlrev_b32_e32 v180, 16, v24
	v_and_b32_e32 v181, 0xffff0000, v24
	v_lshlrev_b32_e32 v182, 16, v25
	v_and_b32_e32 v183, 0xffff0000, v25
	v_readlane_b32 s10, v210, 0
	v_readlane_b32 s9, v211, 0
	s_bitcmp1_b32 s10, 0
	s_cbranch_scc0 .Lcb_s0_0
	v_cvt_pk_f32_fp8_e32 v[184:185], v72
	v_cvt_pk_f32_fp8_sdwa v[186:187], v72 src0_sel:WORD_1
	s_nop 0
	v_pk_fma_f32 v[168:169], v[184:185], s[6:7], v[168:169] op_sel_hi:[1,0,1]
	v_pk_fma_f32 v[170:171], v[186:187], s[6:7], v[170:171] op_sel_hi:[1,0,1]
	v_cvt_pk_f32_fp8_e32 v[188:189], v73
	v_cvt_pk_f32_fp8_sdwa v[190:191], v73 src0_sel:WORD_1
	s_nop 0
	v_pk_fma_f32 v[172:173], v[188:189], s[6:7], v[172:173] op_sel_hi:[1,0,1]
	v_pk_fma_f32 v[174:175], v[190:191], s[6:7], v[174:175] op_sel_hi:[1,0,1]
	v_cvt_pk_f32_fp8_e32 v[184:185], v74
	v_cvt_pk_f32_fp8_sdwa v[186:187], v74 src0_sel:WORD_1
	s_nop 0
	v_pk_fma_f32 v[176:177], v[184:185], s[6:7], v[176:177] op_sel_hi:[1,0,1]
	v_pk_fma_f32 v[178:179], v[186:187], s[6:7], v[178:179] op_sel_hi:[1,0,1]
	v_cvt_pk_f32_fp8_e32 v[188:189], v75
	v_cvt_pk_f32_fp8_sdwa v[190:191], v75 src0_sel:WORD_1
	s_nop 0
	v_pk_fma_f32 v[180:181], v[188:189], s[6:7], v[180:181] op_sel_hi:[1,0,1]
	v_pk_fma_f32 v[182:183], v[190:191], s[6:7], v[182:183] op_sel_hi:[1,0,1]
.Lcb_s0_0:
	s_bitcmp1_b32 s10, 1
	s_cbranch_scc0 .Lcb_s0_1
	v_cvt_pk_f32_fp8_e32 v[184:185], v76
	v_cvt_pk_f32_fp8_sdwa v[186:187], v76 src0_sel:WORD_1
	s_nop 0
	v_pk_fma_f32 v[168:169], v[184:185], s[6:7], v[168:169] op_sel_hi:[1,0,1]
	v_pk_fma_f32 v[170:171], v[186:187], s[6:7], v[170:171] op_sel_hi:[1,0,1]
	v_cvt_pk_f32_fp8_e32 v[188:189], v77
	v_cvt_pk_f32_fp8_sdwa v[190:191], v77 src0_sel:WORD_1
	s_nop 0
	v_pk_fma_f32 v[172:173], v[188:189], s[6:7], v[172:173] op_sel_hi:[1,0,1]
	v_pk_fma_f32 v[174:175], v[190:191], s[6:7], v[174:175] op_sel_hi:[1,0,1]
	v_cvt_pk_f32_fp8_e32 v[184:185], v78
	v_cvt_pk_f32_fp8_sdwa v[186:187], v78 src0_sel:WORD_1
	s_nop 0
	v_pk_fma_f32 v[176:177], v[184:185], s[6:7], v[176:177] op_sel_hi:[1,0,1]
	v_pk_fma_f32 v[178:179], v[186:187], s[6:7], v[178:179] op_sel_hi:[1,0,1]
	v_cvt_pk_f32_fp8_e32 v[188:189], v79
	v_cvt_pk_f32_fp8_sdwa v[190:191], v79 src0_sel:WORD_1
	s_nop 0
	v_pk_fma_f32 v[180:181], v[188:189], s[6:7], v[180:181] op_sel_hi:[1,0,1]
	v_pk_fma_f32 v[182:183], v[190:191], s[6:7], v[182:183] op_sel_hi:[1,0,1]
.Lcb_s0_1:
	s_bitcmp1_b32 s10, 2
	s_cbranch_scc0 .Lcb_s0_2
	v_cvt_pk_f32_fp8_e32 v[184:185], v80
	v_cvt_pk_f32_fp8_sdwa v[186:187], v80 src0_sel:WORD_1
	s_nop 0
	v_pk_fma_f32 v[168:169], v[184:185], s[6:7], v[168:169] op_sel_hi:[1,0,1]
	v_pk_fma_f32 v[170:171], v[186:187], s[6:7], v[170:171] op_sel_hi:[1,0,1]
	v_cvt_pk_f32_fp8_e32 v[188:189], v81
	v_cvt_pk_f32_fp8_sdwa v[190:191], v81 src0_sel:WORD_1
	s_nop 0
	v_pk_fma_f32 v[172:173], v[188:189], s[6:7], v[172:173] op_sel_hi:[1,0,1]
	v_pk_fma_f32 v[174:175], v[190:191], s[6:7], v[174:175] op_sel_hi:[1,0,1]
	v_cvt_pk_f32_fp8_e32 v[184:185], v82
	v_cvt_pk_f32_fp8_sdwa v[186:187], v82 src0_sel:WORD_1
	s_nop 0
	v_pk_fma_f32 v[176:177], v[184:185], s[6:7], v[176:177] op_sel_hi:[1,0,1]
	v_pk_fma_f32 v[178:179], v[186:187], s[6:7], v[178:179] op_sel_hi:[1,0,1]
	v_cvt_pk_f32_fp8_e32 v[188:189], v83
	v_cvt_pk_f32_fp8_sdwa v[190:191], v83 src0_sel:WORD_1
	s_nop 0
	v_pk_fma_f32 v[180:181], v[188:189], s[6:7], v[180:181] op_sel_hi:[1,0,1]
	v_pk_fma_f32 v[182:183], v[190:191], s[6:7], v[182:183] op_sel_hi:[1,0,1]
.Lcb_s0_2:
	s_bitcmp1_b32 s10, 3
	s_cbranch_scc0 .Lcb_s0_3
	v_cvt_pk_f32_fp8_e32 v[184:185], v84
	v_cvt_pk_f32_fp8_sdwa v[186:187], v84 src0_sel:WORD_1
	s_nop 0
	v_pk_fma_f32 v[168:169], v[184:185], s[6:7], v[168:169] op_sel_hi:[1,0,1]
	v_pk_fma_f32 v[170:171], v[186:187], s[6:7], v[170:171] op_sel_hi:[1,0,1]
	v_cvt_pk_f32_fp8_e32 v[188:189], v85
	v_cvt_pk_f32_fp8_sdwa v[190:191], v85 src0_sel:WORD_1
	s_nop 0
	v_pk_fma_f32 v[172:173], v[188:189], s[6:7], v[172:173] op_sel_hi:[1,0,1]
	v_pk_fma_f32 v[174:175], v[190:191], s[6:7], v[174:175] op_sel_hi:[1,0,1]
	v_cvt_pk_f32_fp8_e32 v[184:185], v86
	v_cvt_pk_f32_fp8_sdwa v[186:187], v86 src0_sel:WORD_1
	s_nop 0
	v_pk_fma_f32 v[176:177], v[184:185], s[6:7], v[176:177] op_sel_hi:[1,0,1]
	v_pk_fma_f32 v[178:179], v[186:187], s[6:7], v[178:179] op_sel_hi:[1,0,1]
	v_cvt_pk_f32_fp8_e32 v[188:189], v87
	v_cvt_pk_f32_fp8_sdwa v[190:191], v87 src0_sel:WORD_1
	s_nop 0
	v_pk_fma_f32 v[180:181], v[188:189], s[6:7], v[180:181] op_sel_hi:[1,0,1]
	v_pk_fma_f32 v[182:183], v[190:191], s[6:7], v[182:183] op_sel_hi:[1,0,1]
.Lcb_s0_3:
	s_bitcmp1_b32 s10, 4
	s_cbranch_scc0 .Lcb_s0_4
	v_cvt_pk_f32_fp8_e32 v[184:185], v88
	v_cvt_pk_f32_fp8_sdwa v[186:187], v88 src0_sel:WORD_1
	s_nop 0
	v_pk_fma_f32 v[168:169], v[184:185], s[6:7], v[168:169] op_sel_hi:[1,0,1]
	v_pk_fma_f32 v[170:171], v[186:187], s[6:7], v[170:171] op_sel_hi:[1,0,1]
	v_cvt_pk_f32_fp8_e32 v[188:189], v89
	v_cvt_pk_f32_fp8_sdwa v[190:191], v89 src0_sel:WORD_1
	s_nop 0
	v_pk_fma_f32 v[172:173], v[188:189], s[6:7], v[172:173] op_sel_hi:[1,0,1]
	v_pk_fma_f32 v[174:175], v[190:191], s[6:7], v[174:175] op_sel_hi:[1,0,1]
	v_cvt_pk_f32_fp8_e32 v[184:185], v90
	v_cvt_pk_f32_fp8_sdwa v[186:187], v90 src0_sel:WORD_1
	s_nop 0
	v_pk_fma_f32 v[176:177], v[184:185], s[6:7], v[176:177] op_sel_hi:[1,0,1]
	v_pk_fma_f32 v[178:179], v[186:187], s[6:7], v[178:179] op_sel_hi:[1,0,1]
	v_cvt_pk_f32_fp8_e32 v[188:189], v91
	v_cvt_pk_f32_fp8_sdwa v[190:191], v91 src0_sel:WORD_1
	s_nop 0
	v_pk_fma_f32 v[180:181], v[188:189], s[6:7], v[180:181] op_sel_hi:[1,0,1]
	v_pk_fma_f32 v[182:183], v[190:191], s[6:7], v[182:183] op_sel_hi:[1,0,1]
.Lcb_s0_4:
	s_bitcmp1_b32 s10, 5
	s_cbranch_scc0 .Lcb_s0_5
	v_cvt_pk_f32_fp8_e32 v[184:185], v92
	v_cvt_pk_f32_fp8_sdwa v[186:187], v92 src0_sel:WORD_1
	s_nop 0
	v_pk_fma_f32 v[168:169], v[184:185], s[6:7], v[168:169] op_sel_hi:[1,0,1]
	v_pk_fma_f32 v[170:171], v[186:187], s[6:7], v[170:171] op_sel_hi:[1,0,1]
	v_cvt_pk_f32_fp8_e32 v[188:189], v93
	v_cvt_pk_f32_fp8_sdwa v[190:191], v93 src0_sel:WORD_1
	s_nop 0
	v_pk_fma_f32 v[172:173], v[188:189], s[6:7], v[172:173] op_sel_hi:[1,0,1]
	v_pk_fma_f32 v[174:175], v[190:191], s[6:7], v[174:175] op_sel_hi:[1,0,1]
	v_cvt_pk_f32_fp8_e32 v[184:185], v94
	v_cvt_pk_f32_fp8_sdwa v[186:187], v94 src0_sel:WORD_1
	s_nop 0
	v_pk_fma_f32 v[176:177], v[184:185], s[6:7], v[176:177] op_sel_hi:[1,0,1]
	v_pk_fma_f32 v[178:179], v[186:187], s[6:7], v[178:179] op_sel_hi:[1,0,1]
	v_cvt_pk_f32_fp8_e32 v[188:189], v95
	v_cvt_pk_f32_fp8_sdwa v[190:191], v95 src0_sel:WORD_1
	s_nop 0
	v_pk_fma_f32 v[180:181], v[188:189], s[6:7], v[180:181] op_sel_hi:[1,0,1]
	v_pk_fma_f32 v[182:183], v[190:191], s[6:7], v[182:183] op_sel_hi:[1,0,1]
.Lcb_s0_5:
	s_cmp_lg_u32 s9, 0
	s_cbranch_scc0 .Lcb_ov_done0
.Lcb_ov0:
	s_ff1_i32_b32 s26, s9
	s_add_i32 s27, s9, -1
	v_readlane_b32 s26, v66, s26
	s_and_b32 s9, s9, s27
	s_lshl_b32 s26, s26, 10
	s_add_u32 s26, s4, s26
	s_addc_u32 s27, s5, 0
	global_load_dwordx4 v[200:203], v212, s[26:27] nt
	s_waitcnt vmcnt(0)
	v_cvt_pk_f32_fp8_e32 v[184:185], v200
	v_cvt_pk_f32_fp8_sdwa v[186:187], v200 src0_sel:WORD_1
	s_nop 0
	v_pk_fma_f32 v[168:169], v[184:185], s[6:7], v[168:169] op_sel_hi:[1,0,1]
	v_pk_fma_f32 v[170:171], v[186:187], s[6:7], v[170:171] op_sel_hi:[1,0,1]
	v_cvt_pk_f32_fp8_e32 v[188:189], v201
	v_cvt_pk_f32_fp8_sdwa v[190:191], v201 src0_sel:WORD_1
	s_nop 0
	v_pk_fma_f32 v[172:173], v[188:189], s[6:7], v[172:173] op_sel_hi:[1,0,1]
	v_pk_fma_f32 v[174:175], v[190:191], s[6:7], v[174:175] op_sel_hi:[1,0,1]
	v_cvt_pk_f32_fp8_e32 v[184:185], v202
	v_cvt_pk_f32_fp8_sdwa v[186:187], v202 src0_sel:WORD_1
	s_nop 0
	v_pk_fma_f32 v[176:177], v[184:185], s[6:7], v[176:177] op_sel_hi:[1,0,1]
	v_pk_fma_f32 v[178:179], v[186:187], s[6:7], v[178:179] op_sel_hi:[1,0,1]
	v_cvt_pk_f32_fp8_e32 v[188:189], v203
	v_cvt_pk_f32_fp8_sdwa v[190:191], v203 src0_sel:WORD_1
	s_nop 0
	v_pk_fma_f32 v[180:181], v[188:189], s[6:7], v[180:181] op_sel_hi:[1,0,1]
	v_pk_fma_f32 v[182:183], v[190:191], s[6:7], v[182:183] op_sel_hi:[1,0,1]
	s_cmp_lg_u32 s9, 0
	s_cbranch_scc1 .Lcb_ov0
.Lcb_ov_done0:
	s_mov_b32 s9, s8
	s_cmp_eq_u32 s52, 3
	s_cbranch_scc0 .Lcb_mid0
	s_lshl_b32 s10, s9, 12
	s_add_u32 s12, s14, s10
	s_addc_u32 s13, s15, 0
	global_store_dwordx4 v214, v[168:171], s[12:13]
	global_store_dwordx4 v214, v[172:175], s[12:13] offset:16
	global_store_dwordx4 v214, v[176:179], s[12:13] offset:32
	global_store_dwordx4 v214, v[180:183], s[12:13] offset:48
	s_branch .Lcb_done0
.Lcb_mid0:
	v_cvt_pk_bf16_f32 v192, v168, v169
	v_cvt_pk_bf16_f32 v193, v170, v171
	v_cvt_pk_bf16_f32 v194, v172, v173
	v_cvt_pk_bf16_f32 v195, v174, v175
	v_cvt_pk_bf16_f32 v196, v176, v177
	v_cvt_pk_bf16_f32 v197, v178, v179
	v_cvt_pk_bf16_f32 v198, v180, v181
	v_cvt_pk_bf16_f32 v199, v182, v183
	s_lshl_b32 s10, s9, 11
	s_add_u32 s12, s0, 0x3be00000
	s_addc_u32 s13, s1, 0
	s_add_u32 s12, s12, s10
	s_addc_u32 s13, s13, 0
	global_store_dwordx4 v213, v[192:195], s[12:13]
	global_store_dwordx4 v213, v[196:199], s[12:13] offset:16
	v_mul_f32_e32 v204, v169, v169
	v_mul_f32_e32 v206, v171, v171
	v_fmac_f32_e32 v204, v168, v168
	v_fmac_f32_e32 v206, v170, v170
	v_add_f32_e32 v204, v204, v206
	v_mul_f32_e32 v205, v173, v173
	v_mul_f32_e32 v206, v175, v175
	v_fmac_f32_e32 v205, v172, v172
	v_fmac_f32_e32 v206, v174, v174
	v_add_f32_e32 v205, v205, v206
	v_add_f32_e32 v204, v204, v205
	v_mul_f32_e32 v205, v177, v177
	v_mul_f32_e32 v206, v179, v179
	v_fmac_f32_e32 v205, v176, v176
	v_fmac_f32_e32 v206, v178, v178
	v_add_f32_e32 v205, v205, v206
	v_add_f32_e32 v204, v204, v205
	v_mul_f32_e32 v205, v181, v181
	v_mul_f32_e32 v206, v183, v183
	v_fmac_f32_e32 v205, v180, v180
	v_fmac_f32_e32 v206, v182, v182
	v_add_f32_e32 v205, v205, v206
	v_add_f32_e32 v204, v204, v205
	s_nop 1
	v_add_f32_dpp v204, v204, v204 quad_perm:[1,0,3,2] row_mask:0xf bank_mask:0xf bound_ctrl:1
	s_nop 1
	v_add_f32_dpp v204, v204, v204 quad_perm:[2,3,0,1] row_mask:0xf bank_mask:0xf bound_ctrl:1
	s_nop 1
	v_add_f32_dpp v204, v204, v204 row_half_mirror row_mask:0xf bank_mask:0xf bound_ctrl:1
	s_nop 1
	v_add_f32_dpp v204, v204, v204 row_mirror row_mask:0xf bank_mask:0xf bound_ctrl:1
	s_nop 1
	v_mov_b32_e32 v205, v204
	s_nop 1
	v_permlane16_swap_b32_e32 v204, v205
	s_nop 1
	v_add_f32_e32 v204, v204, v205
	v_mov_b32_e32 v205, v204
	s_nop 1
	v_permlane32_swap_b32_e32 v204, v205
	s_nop 1
	v_add_f32_e32 v204, v204, v205
	v_add_f32_e32 v204, 0x3a8637bd, v204
	v_mul_f32_e32 v204, 0x3a800000, v204
	v_rsq_f32_e32 v208, v204
	s_bitcmp1_b32 s52, 0
	s_cbranch_scc0 .Lcb_f8_0
	s_nop 0
	v_pk_mul_f32 v[168:169], v[168:169], v[208:209] op_sel_hi:[1,0]
	v_pk_mul_f32 v[170:171], v[170:171], v[208:209] op_sel_hi:[1,0]
	v_pk_mul_f32 v[172:173], v[172:173], v[208:209] op_sel_hi:[1,0]
	v_pk_mul_f32 v[174:175], v[174:175], v[208:209] op_sel_hi:[1,0]
	v_pk_mul_f32 v[176:177], v[176:177], v[208:209] op_sel_hi:[1,0]
	v_pk_mul_f32 v[178:179], v[178:179], v[208:209] op_sel_hi:[1,0]
	v_pk_mul_f32 v[180:181], v[180:181], v[208:209] op_sel_hi:[1,0]
	v_pk_mul_f32 v[182:183], v[182:183], v[208:209] op_sel_hi:[1,0]
	v_pk_mul_f32 v[168:169], v[168:169], v[2:3]
	v_pk_mul_f32 v[170:171], v[170:171], v[4:5]
	v_pk_mul_f32 v[172:173], v[172:173], v[6:7]
	v_pk_mul_f32 v[174:175], v[174:175], v[8:9]
	v_pk_mul_f32 v[176:177], v[176:177], v[10:11]
	v_pk_mul_f32 v[178:179], v[178:179], v[12:13]
	v_pk_mul_f32 v[180:181], v[180:181], v[14:15]
	v_pk_mul_f32 v[182:183], v[182:183], v[16:17]
	s_nop 0
	v_cvt_pk_bf16_f32 v192, v168, v169
	v_cvt_pk_bf16_f32 v193, v170, v171
	v_cvt_pk_bf16_f32 v194, v172, v173
	v_cvt_pk_bf16_f32 v195, v174, v175
	v_cvt_pk_bf16_f32 v196, v176, v177
	v_cvt_pk_bf16_f32 v197, v178, v179
	v_cvt_pk_bf16_f32 v198, v180, v181
	v_cvt_pk_bf16_f32 v199, v182, v183
	s_add_u32 s12, s0, 0x33900000
	s_addc_u32 s13, s1, 0
	s_add_u32 s12, s12, s10
	s_addc_u32 s13, s13, 0
	global_store_dwordx4 v213, v[192:195], s[12:13]
	global_store_dwordx4 v213, v[196:199], s[12:13] offset:16
	s_branch .Lcb_done0
.Lcb_f8_0:
	s_nop 0
	v_mul_f32_e32 v208, 4.0, v208
	s_nop 0
	v_pk_mul_f32 v[168:169], v[168:169], v[208:209] op_sel_hi:[1,0]
	v_pk_mul_f32 v[170:171], v[170:171], v[208:209] op_sel_hi:[1,0]
	v_pk_mul_f32 v[172:173], v[172:173], v[208:209] op_sel_hi:[1,0]
	v_pk_mul_f32 v[174:175], v[174:175], v[208:209] op_sel_hi:[1,0]
	v_pk_mul_f32 v[176:177], v[176:177], v[208:209] op_sel_hi:[1,0]
	v_pk_mul_f32 v[178:179], v[178:179], v[208:209] op_sel_hi:[1,0]
	v_pk_mul_f32 v[180:181], v[180:181], v[208:209] op_sel_hi:[1,0]
	v_pk_mul_f32 v[182:183], v[182:183], v[208:209] op_sel_hi:[1,0]
	v_pk_mul_f32 v[168:169], v[168:169], v[2:3]
	v_pk_mul_f32 v[170:171], v[170:171], v[4:5]
	v_pk_mul_f32 v[172:173], v[172:173], v[6:7]
	v_pk_mul_f32 v[174:175], v[174:175], v[8:9]
	v_pk_mul_f32 v[176:177], v[176:177], v[10:11]
	v_pk_mul_f32 v[178:179], v[178:179], v[12:13]
	v_pk_mul_f32 v[180:181], v[180:181], v[14:15]
	v_pk_mul_f32 v[182:183], v[182:183], v[16:17]
	s_nop 0
	v_min_f32_e64 v184, |v168|, s33
	v_bfi_b32 v168, s2, v184, v168
	v_min_f32_e64 v185, |v169|, s33
	v_bfi_b32 v169, s2, v185, v169
	v_min_f32_e64 v186, |v170|, s33
	v_bfi_b32 v170, s2, v186, v170
	v_min_f32_e64 v187, |v171|, s33
	v_bfi_b32 v171, s2, v187, v171
	v_min_f32_e64 v188, |v172|, s33
	v_bfi_b32 v172, s2, v188, v172
	v_min_f32_e64 v189, |v173|, s33
	v_bfi_b32 v173, s2, v189, v173
	v_min_f32_e64 v190, |v174|, s33
	v_bfi_b32 v174, s2, v190, v174
	v_min_f32_e64 v191, |v175|, s33
	v_bfi_b32 v175, s2, v191, v175
	v_min_f32_e64 v184, |v176|, s33
	v_bfi_b32 v176, s2, v184, v176
	v_min_f32_e64 v185, |v177|, s33
	v_bfi_b32 v177, s2, v185, v177
	v_min_f32_e64 v186, |v178|, s33
	v_bfi_b32 v178, s2, v186, v178
	v_min_f32_e64 v187, |v179|, s33
	v_bfi_b32 v179, s2, v187, v179
	v_min_f32_e64 v188, |v180|, s33
	v_bfi_b32 v180, s2, v188, v180
	v_min_f32_e64 v189, |v181|, s33
	v_bfi_b32 v181, s2, v189, v181
	v_min_f32_e64 v190, |v182|, s33
	v_bfi_b32 v182, s2, v190, v182
	v_min_f32_e64 v191, |v183|, s33
	v_bfi_b32 v183, s2, v191, v183
	v_cvt_pk_fp8_f32 v192, v168, v169
	v_cvt_pk_fp8_f32 v193, v172, v173
	v_cvt_pk_fp8_f32 v194, v176, v177
	v_cvt_pk_fp8_f32 v195, v180, v181
	v_cvt_pk_fp8_f32 v192, v170, v171 op_sel:[0,0,1]
	v_cvt_pk_fp8_f32 v193, v174, v175 op_sel:[0,0,1]
	v_cvt_pk_fp8_f32 v194, v178, v179 op_sel:[0,0,1]
	v_cvt_pk_fp8_f32 v195, v182, v183 op_sel:[0,0,1]
	s_lshl_b32 s10, s9, 10
	s_add_u32 s12, s0, 0x33900000
	s_addc_u32 s13, s1, 0
	s_add_u32 s12, s12, s10
	s_addc_u32 s13, s13, 0
	global_store_dwordx2 v212, v[192:193], s[12:13]
	global_store_dwordx2 v212, v[194:195], s[12:13] offset:8
.Lcb_done0:
	s_add_i32 s9, s8, 0x3000
	s_lshr_b32 s10, s9, 12
	s_lshl_b32 s10, s10, 18
	s_and_b32 s12, s9, 0xfff
	s_lshl_b32 s12, s12, 2
	s_add_i32 s10, s10, s12
	s_add_u32 s12, s0, 0x37b00000
	s_addc_u32 s13, s1, 0
	s_add_u32 s12, s12, s10
	s_addc_u32 s13, s13, 0
	global_load_dword v66, v215, s[12:13]
	s_lshl_b32 s10, s9, 11
	s_add_u32 s12, s0, 0x37e00000
	s_addc_u32 s13, s1, 0
	s_add_u32 s12, s12, s10
	s_addc_u32 s13, s13, 0
	global_load_dwordx4 v[18:21], v213, s[12:13] nt
	global_load_dwordx4 v[22:25], v213, s[12:13] offset:16 nt
	s_waitcnt vmcnt(34)
	v_cmp_le_i32_e64 s[24:25], 0, v70
	s_mov_b32 s10, 0
	s_and_b32 s9, s24, 0xffff
	s_cmp_lg_u32 s9, 0
	s_cbranch_scc0 .Lcb_n4_0
	s_ff1_i32_b32 s26, s9
	s_add_i32 s27, s9, -1
	v_readlane_b32 s26, v70, s26
	s_and_b32 s9, s9, s27
	s_bitset1_b32 s10, 0
	s_lshl_b32 s26, s26, 10
	s_add_u32 s26, s4, s26
	s_addc_u32 s27, s5, 0
	s_branch .Lcb_l4_0

.Lcb_l4_0:
	global_load_dwordx4 v[72:75], v212, s[26:27] nt
	s_cmp_lg_u32 s9, 0
	s_cbranch_scc0 .Lcb_n4_1
	s_ff1_i32_b32 s26, s9
	s_add_i32 s27, s9, -1
	v_readlane_b32 s26, v70, s26
	s_and_b32 s9, s9, s27
	s_bitset1_b32 s10, 1
	s_lshl_b32 s26, s26, 10
	s_add_u32 s26, s4, s26
	s_addc_u32 s27, s5, 0
	s_branch .Lcb_l4_1

.Lcb_l4_1:
	global_load_dwordx4 v[76:79], v212, s[26:27] nt
	s_cmp_lg_u32 s9, 0
	s_cbranch_scc0 .Lcb_n4_2
	s_ff1_i32_b32 s26, s9
	s_add_i32 s27, s9, -1
	v_readlane_b32 s26, v70, s26
	s_and_b32 s9, s9, s27
	s_bitset1_b32 s10, 2
	s_lshl_b32 s26, s26, 10
	s_add_u32 s26, s4, s26
	s_addc_u32 s27, s5, 0
	s_branch .Lcb_l4_2

.Lcb_l4_2:
	global_load_dwordx4 v[80:83], v212, s[26:27] nt
	s_cmp_lg_u32 s9, 0
	s_cbranch_scc0 .Lcb_n4_3
	s_ff1_i32_b32 s26, s9
	s_add_i32 s27, s9, -1
	v_readlane_b32 s26, v70, s26
	s_and_b32 s9, s9, s27
	s_bitset1_b32 s10, 3
	s_lshl_b32 s26, s26, 10
	s_add_u32 s26, s4, s26
	s_addc_u32 s27, s5, 0
	s_branch .Lcb_l4_3

.Lcb_l4_3:
	global_load_dwordx4 v[84:87], v212, s[26:27] nt
	s_cmp_lg_u32 s9, 0
	s_cbranch_scc0 .Lcb_n4_4
	s_ff1_i32_b32 s26, s9
	s_add_i32 s27, s9, -1
	v_readlane_b32 s26, v70, s26
	s_and_b32 s9, s9, s27
	s_bitset1_b32 s10, 4
	s_lshl_b32 s26, s26, 10
	s_add_u32 s26, s4, s26
	s_addc_u32 s27, s5, 0
	s_branch .Lcb_l4_4

.Lcb_l4_4:
	global_load_dwordx4 v[88:91], v212, s[26:27] nt
	s_cmp_lg_u32 s9, 0
	s_cbranch_scc0 .Lcb_n4_5
	s_ff1_i32_b32 s26, s9
	s_add_i32 s27, s9, -1
	v_readlane_b32 s26, v70, s26
	s_and_b32 s9, s9, s27
	s_bitset1_b32 s10, 5
	s_lshl_b32 s26, s26, 10
	s_add_u32 s26, s4, s26
	s_addc_u32 s27, s5, 0
	s_branch .Lcb_l4_5

.Lcb_l4_5:
	global_load_dwordx4 v[92:95], v212, s[26:27] nt
	v_writelane_b32 v210, s10, 4
	v_writelane_b32 v211, s9, 4
	s_waitcnt vmcnt(25)
	v_lshlrev_b32_e32 v168, 16, v26
	v_and_b32_e32 v169, 0xffff0000, v26
	v_lshlrev_b32_e32 v170, 16, v27
	v_and_b32_e32 v171, 0xffff0000, v27
	v_lshlrev_b32_e32 v172, 16, v28
	v_and_b32_e32 v173, 0xffff0000, v28
	v_lshlrev_b32_e32 v174, 16, v29
	v_and_b32_e32 v175, 0xffff0000, v29
	v_lshlrev_b32_e32 v176, 16, v30
	v_and_b32_e32 v177, 0xffff0000, v30
	v_lshlrev_b32_e32 v178, 16, v31
	v_and_b32_e32 v179, 0xffff0000, v31
	v_lshlrev_b32_e32 v180, 16, v32
	v_and_b32_e32 v181, 0xffff0000, v32
	v_lshlrev_b32_e32 v182, 16, v33
	v_and_b32_e32 v183, 0xffff0000, v33
	v_readlane_b32 s10, v210, 1
	v_readlane_b32 s9, v211, 1
	s_bitcmp1_b32 s10, 0
	s_cbranch_scc0 .Lcb_s1_0
	v_cvt_pk_f32_fp8_e32 v[184:185], v96
	v_cvt_pk_f32_fp8_sdwa v[186:187], v96 src0_sel:WORD_1
	s_nop 0
	v_pk_fma_f32 v[168:169], v[184:185], s[6:7], v[168:169] op_sel_hi:[1,0,1]
	v_pk_fma_f32 v[170:171], v[186:187], s[6:7], v[170:171] op_sel_hi:[1,0,1]
	v_cvt_pk_f32_fp8_e32 v[188:189], v97
	v_cvt_pk_f32_fp8_sdwa v[190:191], v97 src0_sel:WORD_1
	s_nop 0
	v_pk_fma_f32 v[172:173], v[188:189], s[6:7], v[172:173] op_sel_hi:[1,0,1]
	v_pk_fma_f32 v[174:175], v[190:191], s[6:7], v[174:175] op_sel_hi:[1,0,1]
	v_cvt_pk_f32_fp8_e32 v[184:185], v98
	v_cvt_pk_f32_fp8_sdwa v[186:187], v98 src0_sel:WORD_1
	s_nop 0
	v_pk_fma_f32 v[176:177], v[184:185], s[6:7], v[176:177] op_sel_hi:[1,0,1]
	v_pk_fma_f32 v[178:179], v[186:187], s[6:7], v[178:179] op_sel_hi:[1,0,1]
	v_cvt_pk_f32_fp8_e32 v[188:189], v99
	v_cvt_pk_f32_fp8_sdwa v[190:191], v99 src0_sel:WORD_1
	s_nop 0
	v_pk_fma_f32 v[180:181], v[188:189], s[6:7], v[180:181] op_sel_hi:[1,0,1]
	v_pk_fma_f32 v[182:183], v[190:191], s[6:7], v[182:183] op_sel_hi:[1,0,1]
.Lcb_s1_0:
	s_bitcmp1_b32 s10, 1
	s_cbranch_scc0 .Lcb_s1_1
	v_cvt_pk_f32_fp8_e32 v[184:185], v100
	v_cvt_pk_f32_fp8_sdwa v[186:187], v100 src0_sel:WORD_1
	s_nop 0
	v_pk_fma_f32 v[168:169], v[184:185], s[6:7], v[168:169] op_sel_hi:[1,0,1]
	v_pk_fma_f32 v[170:171], v[186:187], s[6:7], v[170:171] op_sel_hi:[1,0,1]
	v_cvt_pk_f32_fp8_e32 v[188:189], v101
	v_cvt_pk_f32_fp8_sdwa v[190:191], v101 src0_sel:WORD_1
	s_nop 0
	v_pk_fma_f32 v[172:173], v[188:189], s[6:7], v[172:173] op_sel_hi:[1,0,1]
	v_pk_fma_f32 v[174:175], v[190:191], s[6:7], v[174:175] op_sel_hi:[1,0,1]
	v_cvt_pk_f32_fp8_e32 v[184:185], v102
	v_cvt_pk_f32_fp8_sdwa v[186:187], v102 src0_sel:WORD_1
	s_nop 0
	v_pk_fma_f32 v[176:177], v[184:185], s[6:7], v[176:177] op_sel_hi:[1,0,1]
	v_pk_fma_f32 v[178:179], v[186:187], s[6:7], v[178:179] op_sel_hi:[1,0,1]
	v_cvt_pk_f32_fp8_e32 v[188:189], v103
	v_cvt_pk_f32_fp8_sdwa v[190:191], v103 src0_sel:WORD_1
	s_nop 0
	v_pk_fma_f32 v[180:181], v[188:189], s[6:7], v[180:181] op_sel_hi:[1,0,1]
	v_pk_fma_f32 v[182:183], v[190:191], s[6:7], v[182:183] op_sel_hi:[1,0,1]
.Lcb_s1_1:
	s_bitcmp1_b32 s10, 2
	s_cbranch_scc0 .Lcb_s1_2
	v_cvt_pk_f32_fp8_e32 v[184:185], v104
	v_cvt_pk_f32_fp8_sdwa v[186:187], v104 src0_sel:WORD_1
	s_nop 0
	v_pk_fma_f32 v[168:169], v[184:185], s[6:7], v[168:169] op_sel_hi:[1,0,1]
	v_pk_fma_f32 v[170:171], v[186:187], s[6:7], v[170:171] op_sel_hi:[1,0,1]
	v_cvt_pk_f32_fp8_e32 v[188:189], v105
	v_cvt_pk_f32_fp8_sdwa v[190:191], v105 src0_sel:WORD_1
	s_nop 0
	v_pk_fma_f32 v[172:173], v[188:189], s[6:7], v[172:173] op_sel_hi:[1,0,1]
	v_pk_fma_f32 v[174:175], v[190:191], s[6:7], v[174:175] op_sel_hi:[1,0,1]
	v_cvt_pk_f32_fp8_e32 v[184:185], v106
	v_cvt_pk_f32_fp8_sdwa v[186:187], v106 src0_sel:WORD_1
	s_nop 0
	v_pk_fma_f32 v[176:177], v[184:185], s[6:7], v[176:177] op_sel_hi:[1,0,1]
	v_pk_fma_f32 v[178:179], v[186:187], s[6:7], v[178:179] op_sel_hi:[1,0,1]
	v_cvt_pk_f32_fp8_e32 v[188:189], v107
	v_cvt_pk_f32_fp8_sdwa v[190:191], v107 src0_sel:WORD_1
	s_nop 0
	v_pk_fma_f32 v[180:181], v[188:189], s[6:7], v[180:181] op_sel_hi:[1,0,1]
	v_pk_fma_f32 v[182:183], v[190:191], s[6:7], v[182:183] op_sel_hi:[1,0,1]
.Lcb_s1_2:
	s_bitcmp1_b32 s10, 3
	s_cbranch_scc0 .Lcb_s1_3
	v_cvt_pk_f32_fp8_e32 v[184:185], v108
	v_cvt_pk_f32_fp8_sdwa v[186:187], v108 src0_sel:WORD_1
	s_nop 0
	v_pk_fma_f32 v[168:169], v[184:185], s[6:7], v[168:169] op_sel_hi:[1,0,1]
	v_pk_fma_f32 v[170:171], v[186:187], s[6:7], v[170:171] op_sel_hi:[1,0,1]
	v_cvt_pk_f32_fp8_e32 v[188:189], v109
	v_cvt_pk_f32_fp8_sdwa v[190:191], v109 src0_sel:WORD_1
	s_nop 0
	v_pk_fma_f32 v[172:173], v[188:189], s[6:7], v[172:173] op_sel_hi:[1,0,1]
	v_pk_fma_f32 v[174:175], v[190:191], s[6:7], v[174:175] op_sel_hi:[1,0,1]
	v_cvt_pk_f32_fp8_e32 v[184:185], v110
	v_cvt_pk_f32_fp8_sdwa v[186:187], v110 src0_sel:WORD_1
	s_nop 0
	v_pk_fma_f32 v[176:177], v[184:185], s[6:7], v[176:177] op_sel_hi:[1,0,1]
	v_pk_fma_f32 v[178:179], v[186:187], s[6:7], v[178:179] op_sel_hi:[1,0,1]
	v_cvt_pk_f32_fp8_e32 v[188:189], v111
	v_cvt_pk_f32_fp8_sdwa v[190:191], v111 src0_sel:WORD_1
	s_nop 0
	v_pk_fma_f32 v[180:181], v[188:189], s[6:7], v[180:181] op_sel_hi:[1,0,1]
	v_pk_fma_f32 v[182:183], v[190:191], s[6:7], v[182:183] op_sel_hi:[1,0,1]
.Lcb_s1_3:
	s_bitcmp1_b32 s10, 4
	s_cbranch_scc0 .Lcb_s1_4
	v_cvt_pk_f32_fp8_e32 v[184:185], v112
	v_cvt_pk_f32_fp8_sdwa v[186:187], v112 src0_sel:WORD_1
	s_nop 0
	v_pk_fma_f32 v[168:169], v[184:185], s[6:7], v[168:169] op_sel_hi:[1,0,1]
	v_pk_fma_f32 v[170:171], v[186:187], s[6:7], v[170:171] op_sel_hi:[1,0,1]
	v_cvt_pk_f32_fp8_e32 v[188:189], v113
	v_cvt_pk_f32_fp8_sdwa v[190:191], v113 src0_sel:WORD_1
	s_nop 0
	v_pk_fma_f32 v[172:173], v[188:189], s[6:7], v[172:173] op_sel_hi:[1,0,1]
	v_pk_fma_f32 v[174:175], v[190:191], s[6:7], v[174:175] op_sel_hi:[1,0,1]
	v_cvt_pk_f32_fp8_e32 v[184:185], v114
	v_cvt_pk_f32_fp8_sdwa v[186:187], v114 src0_sel:WORD_1
	s_nop 0
	v_pk_fma_f32 v[176:177], v[184:185], s[6:7], v[176:177] op_sel_hi:[1,0,1]
	v_pk_fma_f32 v[178:179], v[186:187], s[6:7], v[178:179] op_sel_hi:[1,0,1]
	v_cvt_pk_f32_fp8_e32 v[188:189], v115
	v_cvt_pk_f32_fp8_sdwa v[190:191], v115 src0_sel:WORD_1
	s_nop 0
	v_pk_fma_f32 v[180:181], v[188:189], s[6:7], v[180:181] op_sel_hi:[1,0,1]
	v_pk_fma_f32 v[182:183], v[190:191], s[6:7], v[182:183] op_sel_hi:[1,0,1]
.Lcb_s1_4:
	s_bitcmp1_b32 s10, 5
	s_cbranch_scc0 .Lcb_s1_5
	v_cvt_pk_f32_fp8_e32 v[184:185], v116
	v_cvt_pk_f32_fp8_sdwa v[186:187], v116 src0_sel:WORD_1
	s_nop 0
	v_pk_fma_f32 v[168:169], v[184:185], s[6:7], v[168:169] op_sel_hi:[1,0,1]
	v_pk_fma_f32 v[170:171], v[186:187], s[6:7], v[170:171] op_sel_hi:[1,0,1]
	v_cvt_pk_f32_fp8_e32 v[188:189], v117
	v_cvt_pk_f32_fp8_sdwa v[190:191], v117 src0_sel:WORD_1
	s_nop 0
	v_pk_fma_f32 v[172:173], v[188:189], s[6:7], v[172:173] op_sel_hi:[1,0,1]
	v_pk_fma_f32 v[174:175], v[190:191], s[6:7], v[174:175] op_sel_hi:[1,0,1]
	v_cvt_pk_f32_fp8_e32 v[184:185], v118
	v_cvt_pk_f32_fp8_sdwa v[186:187], v118 src0_sel:WORD_1
	s_nop 0
	v_pk_fma_f32 v[176:177], v[184:185], s[6:7], v[176:177] op_sel_hi:[1,0,1]
	v_pk_fma_f32 v[178:179], v[186:187], s[6:7], v[178:179] op_sel_hi:[1,0,1]
	v_cvt_pk_f32_fp8_e32 v[188:189], v119
	v_cvt_pk_f32_fp8_sdwa v[190:191], v119 src0_sel:WORD_1
	s_nop 0
	v_pk_fma_f32 v[180:181], v[188:189], s[6:7], v[180:181] op_sel_hi:[1,0,1]
	v_pk_fma_f32 v[182:183], v[190:191], s[6:7], v[182:183] op_sel_hi:[1,0,1]

.Lcb_ov1:
	s_ff1_i32_b32 s26, s9
	s_add_i32 s27, s9, -1
	v_readlane_b32 s26, v67, s26
	s_and_b32 s9, s9, s27
	s_lshl_b32 s26, s26, 10
	s_add_u32 s26, s4, s26
	s_addc_u32 s27, s5, 0
	global_load_dwordx4 v[200:203], v212, s[26:27] nt
	s_waitcnt vmcnt(0)
	v_cvt_pk_f32_fp8_e32 v[184:185], v200
	v_cvt_pk_f32_fp8_sdwa v[186:187], v200 src0_sel:WORD_1
	s_nop 0
	v_pk_fma_f32 v[168:169], v[184:185], s[6:7], v[168:169] op_sel_hi:[1,0,1]
	v_pk_fma_f32 v[170:171], v[186:187], s[6:7], v[170:171] op_sel_hi:[1,0,1]
	v_cvt_pk_f32_fp8_e32 v[188:189], v201
	v_cvt_pk_f32_fp8_sdwa v[190:191], v201 src0_sel:WORD_1
	s_nop 0
	v_pk_fma_f32 v[172:173], v[188:189], s[6:7], v[172:173] op_sel_hi:[1,0,1]
	v_pk_fma_f32 v[174:175], v[190:191], s[6:7], v[174:175] op_sel_hi:[1,0,1]
	v_cvt_pk_f32_fp8_e32 v[184:185], v202
	v_cvt_pk_f32_fp8_sdwa v[186:187], v202 src0_sel:WORD_1
	s_nop 0
	v_pk_fma_f32 v[176:177], v[184:185], s[6:7], v[176:177] op_sel_hi:[1,0,1]
	v_pk_fma_f32 v[178:179], v[186:187], s[6:7], v[178:179] op_sel_hi:[1,0,1]
	v_cvt_pk_f32_fp8_e32 v[188:189], v203
	v_cvt_pk_f32_fp8_sdwa v[190:191], v203 src0_sel:WORD_1
	s_nop 0
	v_pk_fma_f32 v[180:181], v[188:189], s[6:7], v[180:181] op_sel_hi:[1,0,1]
	v_pk_fma_f32 v[182:183], v[190:191], s[6:7], v[182:183] op_sel_hi:[1,0,1]
	s_cmp_lg_u32 s9, 0
	s_cbranch_scc1 .Lcb_ov1
.Lcb_ov_done1:
	s_add_i32 s9, s8, 0x800
	s_cmp_eq_u32 s52, 3
	s_cbranch_scc0 .Lcb_mid1
	s_lshl_b32 s10, s9, 12
	s_add_u32 s12, s14, s10
	s_addc_u32 s13, s15, 0
	global_store_dwordx4 v214, v[168:171], s[12:13]
	global_store_dwordx4 v214, v[172:175], s[12:13] offset:16
	global_store_dwordx4 v214, v[176:179], s[12:13] offset:32
	global_store_dwordx4 v214, v[180:183], s[12:13] offset:48
	s_branch .Lcb_done1

.Lcb_done1:
	s_add_i32 s9, s8, 0x3800
	s_lshr_b32 s10, s9, 12
	s_lshl_b32 s10, s10, 18
	s_and_b32 s12, s9, 0xfff
	s_lshl_b32 s12, s12, 2
	s_add_i32 s10, s10, s12
	s_add_u32 s12, s0, 0x37b00000
	s_addc_u32 s13, s1, 0
	s_add_u32 s12, s12, s10
	s_addc_u32 s13, s13, 0
	global_load_dword v67, v215, s[12:13]
	s_lshl_b32 s10, s9, 11
	s_add_u32 s12, s0, 0x37e00000
	s_addc_u32 s13, s1, 0
	s_add_u32 s12, s12, s10
	s_addc_u32 s13, s13, 0
	global_load_dwordx4 v[26:29], v213, s[12:13] nt
	global_load_dwordx4 v[30:33], v213, s[12:13] offset:16 nt
	s_waitcnt vmcnt(44)
	v_cmp_le_i32_e64 s[24:25], 0, v71
	s_mov_b32 s10, 0
	s_and_b32 s9, s24, 0xffff
	s_cmp_lg_u32 s9, 0
	s_cbranch_scc0 .Lcb_n5_0
	s_ff1_i32_b32 s26, s9
	s_add_i32 s27, s9, -1
	v_readlane_b32 s26, v71, s26
	s_and_b32 s9, s9, s27
	s_bitset1_b32 s10, 0
	s_lshl_b32 s26, s26, 10
	s_add_u32 s26, s4, s26
	s_addc_u32 s27, s5, 0
	s_branch .Lcb_l5_0

.Lcb_l5_0:
	global_load_dwordx4 v[96:99], v212, s[26:27] nt
	s_cmp_lg_u32 s9, 0
	s_cbranch_scc0 .Lcb_n5_1
	s_ff1_i32_b32 s26, s9
	s_add_i32 s27, s9, -1
	v_readlane_b32 s26, v71, s26
	s_and_b32 s9, s9, s27
	s_bitset1_b32 s10, 1
	s_lshl_b32 s26, s26, 10
	s_add_u32 s26, s4, s26
	s_addc_u32 s27, s5, 0
	s_branch .Lcb_l5_1

.Lcb_l5_1:
	global_load_dwordx4 v[100:103], v212, s[26:27] nt
	s_cmp_lg_u32 s9, 0
	s_cbranch_scc0 .Lcb_n5_2
	s_ff1_i32_b32 s26, s9
	s_add_i32 s27, s9, -1
	v_readlane_b32 s26, v71, s26
	s_and_b32 s9, s9, s27
	s_bitset1_b32 s10, 2
	s_lshl_b32 s26, s26, 10
	s_add_u32 s26, s4, s26
	s_addc_u32 s27, s5, 0
	s_branch .Lcb_l5_2

.Lcb_l5_2:
	global_load_dwordx4 v[104:107], v212, s[26:27] nt
	s_cmp_lg_u32 s9, 0
	s_cbranch_scc0 .Lcb_n5_3
	s_ff1_i32_b32 s26, s9
	s_add_i32 s27, s9, -1
	v_readlane_b32 s26, v71, s26
	s_and_b32 s9, s9, s27
	s_bitset1_b32 s10, 3
	s_lshl_b32 s26, s26, 10
	s_add_u32 s26, s4, s26
	s_addc_u32 s27, s5, 0
	s_branch .Lcb_l5_3

.Lcb_l5_3:
	global_load_dwordx4 v[108:111], v212, s[26:27] nt
	s_cmp_lg_u32 s9, 0
	s_cbranch_scc0 .Lcb_n5_4
	s_ff1_i32_b32 s26, s9
	s_add_i32 s27, s9, -1
	v_readlane_b32 s26, v71, s26
	s_and_b32 s9, s9, s27
	s_bitset1_b32 s10, 4
	s_lshl_b32 s26, s26, 10
	s_add_u32 s26, s4, s26
	s_addc_u32 s27, s5, 0
	s_branch .Lcb_l5_4

.Lcb_l5_4:
	global_load_dwordx4 v[112:115], v212, s[26:27] nt
	s_cmp_lg_u32 s9, 0
	s_cbranch_scc0 .Lcb_n5_5
	s_ff1_i32_b32 s26, s9
	s_add_i32 s27, s9, -1
	v_readlane_b32 s26, v71, s26
	s_and_b32 s9, s9, s27
	s_bitset1_b32 s10, 5
	s_lshl_b32 s26, s26, 10
	s_add_u32 s26, s4, s26
	s_addc_u32 s27, s5, 0
	s_branch .Lcb_l5_5

.Lcb_l5_5:
	global_load_dwordx4 v[116:119], v212, s[26:27] nt
	v_writelane_b32 v210, s10, 5
	v_writelane_b32 v211, s9, 5
	s_waitcnt vmcnt(32)
	v_lshlrev_b32_e32 v168, 16, v34
	v_and_b32_e32 v169, 0xffff0000, v34
	v_lshlrev_b32_e32 v170, 16, v35
	v_and_b32_e32 v171, 0xffff0000, v35
	v_lshlrev_b32_e32 v172, 16, v36
	v_and_b32_e32 v173, 0xffff0000, v36
	v_lshlrev_b32_e32 v174, 16, v37
	v_and_b32_e32 v175, 0xffff0000, v37
	v_lshlrev_b32_e32 v176, 16, v38
	v_and_b32_e32 v177, 0xffff0000, v38
	v_lshlrev_b32_e32 v178, 16, v39
	v_and_b32_e32 v179, 0xffff0000, v39
	v_lshlrev_b32_e32 v180, 16, v40
	v_and_b32_e32 v181, 0xffff0000, v40
	v_lshlrev_b32_e32 v182, 16, v41
	v_and_b32_e32 v183, 0xffff0000, v41
	v_readlane_b32 s10, v210, 2
	v_readlane_b32 s9, v211, 2
	s_bitcmp1_b32 s10, 0
	s_cbranch_scc0 .Lcb_s2_0
	v_cvt_pk_f32_fp8_e32 v[184:185], v120
	v_cvt_pk_f32_fp8_sdwa v[186:187], v120 src0_sel:WORD_1
	s_nop 0
	v_pk_fma_f32 v[168:169], v[184:185], s[6:7], v[168:169] op_sel_hi:[1,0,1]
	v_pk_fma_f32 v[170:171], v[186:187], s[6:7], v[170:171] op_sel_hi:[1,0,1]
	v_cvt_pk_f32_fp8_e32 v[188:189], v121
	v_cvt_pk_f32_fp8_sdwa v[190:191], v121 src0_sel:WORD_1
	s_nop 0
	v_pk_fma_f32 v[172:173], v[188:189], s[6:7], v[172:173] op_sel_hi:[1,0,1]
	v_pk_fma_f32 v[174:175], v[190:191], s[6:7], v[174:175] op_sel_hi:[1,0,1]
	v_cvt_pk_f32_fp8_e32 v[184:185], v122
	v_cvt_pk_f32_fp8_sdwa v[186:187], v122 src0_sel:WORD_1
	s_nop 0
	v_pk_fma_f32 v[176:177], v[184:185], s[6:7], v[176:177] op_sel_hi:[1,0,1]
	v_pk_fma_f32 v[178:179], v[186:187], s[6:7], v[178:179] op_sel_hi:[1,0,1]
	v_cvt_pk_f32_fp8_e32 v[188:189], v123
	v_cvt_pk_f32_fp8_sdwa v[190:191], v123 src0_sel:WORD_1
	s_nop 0
	v_pk_fma_f32 v[180:181], v[188:189], s[6:7], v[180:181] op_sel_hi:[1,0,1]
	v_pk_fma_f32 v[182:183], v[190:191], s[6:7], v[182:183] op_sel_hi:[1,0,1]
.Lcb_s2_0:
	s_bitcmp1_b32 s10, 1
	s_cbranch_scc0 .Lcb_s2_1
	v_cvt_pk_f32_fp8_e32 v[184:185], v124
	v_cvt_pk_f32_fp8_sdwa v[186:187], v124 src0_sel:WORD_1
	s_nop 0
	v_pk_fma_f32 v[168:169], v[184:185], s[6:7], v[168:169] op_sel_hi:[1,0,1]
	v_pk_fma_f32 v[170:171], v[186:187], s[6:7], v[170:171] op_sel_hi:[1,0,1]
	v_cvt_pk_f32_fp8_e32 v[188:189], v125
	v_cvt_pk_f32_fp8_sdwa v[190:191], v125 src0_sel:WORD_1
	s_nop 0
	v_pk_fma_f32 v[172:173], v[188:189], s[6:7], v[172:173] op_sel_hi:[1,0,1]
	v_pk_fma_f32 v[174:175], v[190:191], s[6:7], v[174:175] op_sel_hi:[1,0,1]
	v_cvt_pk_f32_fp8_e32 v[184:185], v126
	v_cvt_pk_f32_fp8_sdwa v[186:187], v126 src0_sel:WORD_1
	s_nop 0
	v_pk_fma_f32 v[176:177], v[184:185], s[6:7], v[176:177] op_sel_hi:[1,0,1]
	v_pk_fma_f32 v[178:179], v[186:187], s[6:7], v[178:179] op_sel_hi:[1,0,1]
	v_cvt_pk_f32_fp8_e32 v[188:189], v127
	v_cvt_pk_f32_fp8_sdwa v[190:191], v127 src0_sel:WORD_1
	s_nop 0
	v_pk_fma_f32 v[180:181], v[188:189], s[6:7], v[180:181] op_sel_hi:[1,0,1]
	v_pk_fma_f32 v[182:183], v[190:191], s[6:7], v[182:183] op_sel_hi:[1,0,1]
.Lcb_s2_1:
	s_bitcmp1_b32 s10, 2
	s_cbranch_scc0 .Lcb_s2_2
	v_cvt_pk_f32_fp8_e32 v[184:185], v128
	v_cvt_pk_f32_fp8_sdwa v[186:187], v128 src0_sel:WORD_1
	s_nop 0
	v_pk_fma_f32 v[168:169], v[184:185], s[6:7], v[168:169] op_sel_hi:[1,0,1]
	v_pk_fma_f32 v[170:171], v[186:187], s[6:7], v[170:171] op_sel_hi:[1,0,1]
	v_cvt_pk_f32_fp8_e32 v[188:189], v129
	v_cvt_pk_f32_fp8_sdwa v[190:191], v129 src0_sel:WORD_1
	s_nop 0
	v_pk_fma_f32 v[172:173], v[188:189], s[6:7], v[172:173] op_sel_hi:[1,0,1]
	v_pk_fma_f32 v[174:175], v[190:191], s[6:7], v[174:175] op_sel_hi:[1,0,1]
	v_cvt_pk_f32_fp8_e32 v[184:185], v130
	v_cvt_pk_f32_fp8_sdwa v[186:187], v130 src0_sel:WORD_1
	s_nop 0
	v_pk_fma_f32 v[176:177], v[184:185], s[6:7], v[176:177] op_sel_hi:[1,0,1]
	v_pk_fma_f32 v[178:179], v[186:187], s[6:7], v[178:179] op_sel_hi:[1,0,1]
	v_cvt_pk_f32_fp8_e32 v[188:189], v131
	v_cvt_pk_f32_fp8_sdwa v[190:191], v131 src0_sel:WORD_1
	s_nop 0
	v_pk_fma_f32 v[180:181], v[188:189], s[6:7], v[180:181] op_sel_hi:[1,0,1]
	v_pk_fma_f32 v[182:183], v[190:191], s[6:7], v[182:183] op_sel_hi:[1,0,1]
.Lcb_s2_2:
	s_bitcmp1_b32 s10, 3
	s_cbranch_scc0 .Lcb_s2_3
	v_cvt_pk_f32_fp8_e32 v[184:185], v132
	v_cvt_pk_f32_fp8_sdwa v[186:187], v132 src0_sel:WORD_1
	s_nop 0
	v_pk_fma_f32 v[168:169], v[184:185], s[6:7], v[168:169] op_sel_hi:[1,0,1]
	v_pk_fma_f32 v[170:171], v[186:187], s[6:7], v[170:171] op_sel_hi:[1,0,1]
	v_cvt_pk_f32_fp8_e32 v[188:189], v133
	v_cvt_pk_f32_fp8_sdwa v[190:191], v133 src0_sel:WORD_1
	s_nop 0
	v_pk_fma_f32 v[172:173], v[188:189], s[6:7], v[172:173] op_sel_hi:[1,0,1]
	v_pk_fma_f32 v[174:175], v[190:191], s[6:7], v[174:175] op_sel_hi:[1,0,1]
	v_cvt_pk_f32_fp8_e32 v[184:185], v134
	v_cvt_pk_f32_fp8_sdwa v[186:187], v134 src0_sel:WORD_1
	s_nop 0
	v_pk_fma_f32 v[176:177], v[184:185], s[6:7], v[176:177] op_sel_hi:[1,0,1]
	v_pk_fma_f32 v[178:179], v[186:187], s[6:7], v[178:179] op_sel_hi:[1,0,1]
	v_cvt_pk_f32_fp8_e32 v[188:189], v135
	v_cvt_pk_f32_fp8_sdwa v[190:191], v135 src0_sel:WORD_1
	s_nop 0
	v_pk_fma_f32 v[180:181], v[188:189], s[6:7], v[180:181] op_sel_hi:[1,0,1]
	v_pk_fma_f32 v[182:183], v[190:191], s[6:7], v[182:183] op_sel_hi:[1,0,1]
.Lcb_s2_3:
	s_bitcmp1_b32 s10, 4
	s_cbranch_scc0 .Lcb_s2_4
	v_cvt_pk_f32_fp8_e32 v[184:185], v136
	v_cvt_pk_f32_fp8_sdwa v[186:187], v136 src0_sel:WORD_1
	s_nop 0
	v_pk_fma_f32 v[168:169], v[184:185], s[6:7], v[168:169] op_sel_hi:[1,0,1]
	v_pk_fma_f32 v[170:171], v[186:187], s[6:7], v[170:171] op_sel_hi:[1,0,1]
	v_cvt_pk_f32_fp8_e32 v[188:189], v137
	v_cvt_pk_f32_fp8_sdwa v[190:191], v137 src0_sel:WORD_1
	s_nop 0
	v_pk_fma_f32 v[172:173], v[188:189], s[6:7], v[172:173] op_sel_hi:[1,0,1]
	v_pk_fma_f32 v[174:175], v[190:191], s[6:7], v[174:175] op_sel_hi:[1,0,1]
	v_cvt_pk_f32_fp8_e32 v[184:185], v138
	v_cvt_pk_f32_fp8_sdwa v[186:187], v138 src0_sel:WORD_1
	s_nop 0
	v_pk_fma_f32 v[176:177], v[184:185], s[6:7], v[176:177] op_sel_hi:[1,0,1]
	v_pk_fma_f32 v[178:179], v[186:187], s[6:7], v[178:179] op_sel_hi:[1,0,1]
	v_cvt_pk_f32_fp8_e32 v[188:189], v139
	v_cvt_pk_f32_fp8_sdwa v[190:191], v139 src0_sel:WORD_1
	s_nop 0
	v_pk_fma_f32 v[180:181], v[188:189], s[6:7], v[180:181] op_sel_hi:[1,0,1]
	v_pk_fma_f32 v[182:183], v[190:191], s[6:7], v[182:183] op_sel_hi:[1,0,1]
.Lcb_s2_4:
	s_bitcmp1_b32 s10, 5
	s_cbranch_scc0 .Lcb_s2_5
	v_cvt_pk_f32_fp8_e32 v[184:185], v140
	v_cvt_pk_f32_fp8_sdwa v[186:187], v140 src0_sel:WORD_1
	s_nop 0
	v_pk_fma_f32 v[168:169], v[184:185], s[6:7], v[168:169] op_sel_hi:[1,0,1]
	v_pk_fma_f32 v[170:171], v[186:187], s[6:7], v[170:171] op_sel_hi:[1,0,1]
	v_cvt_pk_f32_fp8_e32 v[188:189], v141
	v_cvt_pk_f32_fp8_sdwa v[190:191], v141 src0_sel:WORD_1
	s_nop 0
	v_pk_fma_f32 v[172:173], v[188:189], s[6:7], v[172:173] op_sel_hi:[1,0,1]
	v_pk_fma_f32 v[174:175], v[190:191], s[6:7], v[174:175] op_sel_hi:[1,0,1]
	v_cvt_pk_f32_fp8_e32 v[184:185], v142
	v_cvt_pk_f32_fp8_sdwa v[186:187], v142 src0_sel:WORD_1
	s_nop 0
	v_pk_fma_f32 v[176:177], v[184:185], s[6:7], v[176:177] op_sel_hi:[1,0,1]
	v_pk_fma_f32 v[178:179], v[186:187], s[6:7], v[178:179] op_sel_hi:[1,0,1]
	v_cvt_pk_f32_fp8_e32 v[188:189], v143
	v_cvt_pk_f32_fp8_sdwa v[190:191], v143 src0_sel:WORD_1
	s_nop 0
	v_pk_fma_f32 v[180:181], v[188:189], s[6:7], v[180:181] op_sel_hi:[1,0,1]
	v_pk_fma_f32 v[182:183], v[190:191], s[6:7], v[182:183] op_sel_hi:[1,0,1]

.Lcb_ov2:
	s_ff1_i32_b32 s26, s9
	s_add_i32 s27, s9, -1
	v_readlane_b32 s26, v68, s26
	s_and_b32 s9, s9, s27
	s_lshl_b32 s26, s26, 10
	s_add_u32 s26, s4, s26
	s_addc_u32 s27, s5, 0
	global_load_dwordx4 v[200:203], v212, s[26:27] nt
	s_waitcnt vmcnt(0)
	v_cvt_pk_f32_fp8_e32 v[184:185], v200
	v_cvt_pk_f32_fp8_sdwa v[186:187], v200 src0_sel:WORD_1
	s_nop 0
	v_pk_fma_f32 v[168:169], v[184:185], s[6:7], v[168:169] op_sel_hi:[1,0,1]
	v_pk_fma_f32 v[170:171], v[186:187], s[6:7], v[170:171] op_sel_hi:[1,0,1]
	v_cvt_pk_f32_fp8_e32 v[188:189], v201
	v_cvt_pk_f32_fp8_sdwa v[190:191], v201 src0_sel:WORD_1
	s_nop 0
	v_pk_fma_f32 v[172:173], v[188:189], s[6:7], v[172:173] op_sel_hi:[1,0,1]
	v_pk_fma_f32 v[174:175], v[190:191], s[6:7], v[174:175] op_sel_hi:[1,0,1]
	v_cvt_pk_f32_fp8_e32 v[184:185], v202
	v_cvt_pk_f32_fp8_sdwa v[186:187], v202 src0_sel:WORD_1
	s_nop 0
	v_pk_fma_f32 v[176:177], v[184:185], s[6:7], v[176:177] op_sel_hi:[1,0,1]
	v_pk_fma_f32 v[178:179], v[186:187], s[6:7], v[178:179] op_sel_hi:[1,0,1]
	v_cvt_pk_f32_fp8_e32 v[188:189], v203
	v_cvt_pk_f32_fp8_sdwa v[190:191], v203 src0_sel:WORD_1
	s_nop 0
	v_pk_fma_f32 v[180:181], v[188:189], s[6:7], v[180:181] op_sel_hi:[1,0,1]
	v_pk_fma_f32 v[182:183], v[190:191], s[6:7], v[182:183] op_sel_hi:[1,0,1]
	s_cmp_lg_u32 s9, 0
	s_cbranch_scc1 .Lcb_ov2
.Lcb_ov_done2:
	s_add_i32 s9, s8, 0x1000
	s_cmp_eq_u32 s52, 3
	s_cbranch_scc0 .Lcb_mid2
	s_lshl_b32 s10, s9, 12
	s_add_u32 s12, s14, s10
	s_addc_u32 s13, s15, 0
	global_store_dwordx4 v214, v[168:171], s[12:13]
	global_store_dwordx4 v214, v[172:175], s[12:13] offset:16
	global_store_dwordx4 v214, v[176:179], s[12:13] offset:32
	global_store_dwordx4 v214, v[180:183], s[12:13] offset:48
	s_branch .Lcb_done2

.Lcb_done2:
	s_add_i32 s9, s8, 0x4000
	s_lshr_b32 s10, s9, 12
	s_lshl_b32 s10, s10, 18
	s_and_b32 s12, s9, 0xfff
	s_lshl_b32 s12, s12, 2
	s_add_i32 s10, s10, s12
	s_add_u32 s12, s0, 0x37b00000
	s_addc_u32 s13, s1, 0
	s_add_u32 s12, s12, s10
	s_addc_u32 s13, s13, 0
	global_load_dword v68, v215, s[12:13]
	s_lshl_b32 s10, s9, 11
	s_add_u32 s12, s0, 0x37e00000
	s_addc_u32 s13, s1, 0
	s_add_u32 s12, s12, s10
	s_addc_u32 s13, s13, 0
	global_load_dwordx4 v[34:37], v213, s[12:13] nt
	global_load_dwordx4 v[38:41], v213, s[12:13] offset:16 nt
	s_waitcnt vmcnt(26)
	v_cmp_le_i32_e64 s[24:25], 0, v66
	s_mov_b32 s10, 0
	s_and_b32 s9, s24, 0xffff
	s_cmp_lg_u32 s9, 0
	s_cbranch_scc0 .Lcb_n6_0
	s_ff1_i32_b32 s26, s9
	s_add_i32 s27, s9, -1
	v_readlane_b32 s26, v66, s26
	s_and_b32 s9, s9, s27
	s_bitset1_b32 s10, 0
	s_lshl_b32 s26, s26, 10
	s_add_u32 s26, s4, s26
	s_addc_u32 s27, s5, 0
	s_branch .Lcb_l6_0

.Lcb_l6_0:
	global_load_dwordx4 v[120:123], v212, s[26:27] nt
	s_cmp_lg_u32 s9, 0
	s_cbranch_scc0 .Lcb_n6_1
	s_ff1_i32_b32 s26, s9
	s_add_i32 s27, s9, -1
	v_readlane_b32 s26, v66, s26
	s_and_b32 s9, s9, s27
	s_bitset1_b32 s10, 1
	s_lshl_b32 s26, s26, 10
	s_add_u32 s26, s4, s26
	s_addc_u32 s27, s5, 0
	s_branch .Lcb_l6_1

.Lcb_l6_1:
	global_load_dwordx4 v[124:127], v212, s[26:27] nt
	s_cmp_lg_u32 s9, 0
	s_cbranch_scc0 .Lcb_n6_2
	s_ff1_i32_b32 s26, s9
	s_add_i32 s27, s9, -1
	v_readlane_b32 s26, v66, s26
	s_and_b32 s9, s9, s27
	s_bitset1_b32 s10, 2
	s_lshl_b32 s26, s26, 10
	s_add_u32 s26, s4, s26
	s_addc_u32 s27, s5, 0
	s_branch .Lcb_l6_2

.Lcb_l6_2:
	global_load_dwordx4 v[128:131], v212, s[26:27] nt
	s_cmp_lg_u32 s9, 0
	s_cbranch_scc0 .Lcb_n6_3
	s_ff1_i32_b32 s26, s9
	s_add_i32 s27, s9, -1
	v_readlane_b32 s26, v66, s26
	s_and_b32 s9, s9, s27
	s_bitset1_b32 s10, 3
	s_lshl_b32 s26, s26, 10
	s_add_u32 s26, s4, s26
	s_addc_u32 s27, s5, 0
	s_branch .Lcb_l6_3

.Lcb_l6_3:
	global_load_dwordx4 v[132:135], v212, s[26:27] nt
	s_cmp_lg_u32 s9, 0
	s_cbranch_scc0 .Lcb_n6_4
	s_ff1_i32_b32 s26, s9
	s_add_i32 s27, s9, -1
	v_readlane_b32 s26, v66, s26
	s_and_b32 s9, s9, s27
	s_bitset1_b32 s10, 4
	s_lshl_b32 s26, s26, 10
	s_add_u32 s26, s4, s26
	s_addc_u32 s27, s5, 0
	s_branch .Lcb_l6_4

.Lcb_l6_4:
	global_load_dwordx4 v[136:139], v212, s[26:27] nt
	s_cmp_lg_u32 s9, 0
	s_cbranch_scc0 .Lcb_n6_5
	s_ff1_i32_b32 s26, s9
	s_add_i32 s27, s9, -1
	v_readlane_b32 s26, v66, s26
	s_and_b32 s9, s9, s27
	s_bitset1_b32 s10, 5
	s_lshl_b32 s26, s26, 10
	s_add_u32 s26, s4, s26
	s_addc_u32 s27, s5, 0
	s_branch .Lcb_l6_5

.Lcb_l6_5:
	global_load_dwordx4 v[140:143], v212, s[26:27] nt
	v_writelane_b32 v210, s10, 6
	v_writelane_b32 v211, s9, 6
	s_waitcnt vmcnt(39)
	v_lshlrev_b32_e32 v168, 16, v42
	v_and_b32_e32 v169, 0xffff0000, v42
	v_lshlrev_b32_e32 v170, 16, v43
	v_and_b32_e32 v171, 0xffff0000, v43
	v_lshlrev_b32_e32 v172, 16, v44
	v_and_b32_e32 v173, 0xffff0000, v44
	v_lshlrev_b32_e32 v174, 16, v45
	v_and_b32_e32 v175, 0xffff0000, v45
	v_lshlrev_b32_e32 v176, 16, v46
	v_and_b32_e32 v177, 0xffff0000, v46
	v_lshlrev_b32_e32 v178, 16, v47
	v_and_b32_e32 v179, 0xffff0000, v47
	v_lshlrev_b32_e32 v180, 16, v48
	v_and_b32_e32 v181, 0xffff0000, v48
	v_lshlrev_b32_e32 v182, 16, v49
	v_and_b32_e32 v183, 0xffff0000, v49
	v_readlane_b32 s10, v210, 3
	v_readlane_b32 s9, v211, 3
	s_bitcmp1_b32 s10, 0
	s_cbranch_scc0 .Lcb_s3_0
	v_cvt_pk_f32_fp8_e32 v[184:185], v144
	v_cvt_pk_f32_fp8_sdwa v[186:187], v144 src0_sel:WORD_1
	s_nop 0
	v_pk_fma_f32 v[168:169], v[184:185], s[6:7], v[168:169] op_sel_hi:[1,0,1]
	v_pk_fma_f32 v[170:171], v[186:187], s[6:7], v[170:171] op_sel_hi:[1,0,1]
	v_cvt_pk_f32_fp8_e32 v[188:189], v145
	v_cvt_pk_f32_fp8_sdwa v[190:191], v145 src0_sel:WORD_1
	s_nop 0
	v_pk_fma_f32 v[172:173], v[188:189], s[6:7], v[172:173] op_sel_hi:[1,0,1]
	v_pk_fma_f32 v[174:175], v[190:191], s[6:7], v[174:175] op_sel_hi:[1,0,1]
	v_cvt_pk_f32_fp8_e32 v[184:185], v146
	v_cvt_pk_f32_fp8_sdwa v[186:187], v146 src0_sel:WORD_1
	s_nop 0
	v_pk_fma_f32 v[176:177], v[184:185], s[6:7], v[176:177] op_sel_hi:[1,0,1]
	v_pk_fma_f32 v[178:179], v[186:187], s[6:7], v[178:179] op_sel_hi:[1,0,1]
	v_cvt_pk_f32_fp8_e32 v[188:189], v147
	v_cvt_pk_f32_fp8_sdwa v[190:191], v147 src0_sel:WORD_1
	s_nop 0
	v_pk_fma_f32 v[180:181], v[188:189], s[6:7], v[180:181] op_sel_hi:[1,0,1]
	v_pk_fma_f32 v[182:183], v[190:191], s[6:7], v[182:183] op_sel_hi:[1,0,1]
.Lcb_s3_0:
	s_bitcmp1_b32 s10, 1
	s_cbranch_scc0 .Lcb_s3_1
	v_cvt_pk_f32_fp8_e32 v[184:185], v148
	v_cvt_pk_f32_fp8_sdwa v[186:187], v148 src0_sel:WORD_1
	s_nop 0
	v_pk_fma_f32 v[168:169], v[184:185], s[6:7], v[168:169] op_sel_hi:[1,0,1]
	v_pk_fma_f32 v[170:171], v[186:187], s[6:7], v[170:171] op_sel_hi:[1,0,1]
	v_cvt_pk_f32_fp8_e32 v[188:189], v149
	v_cvt_pk_f32_fp8_sdwa v[190:191], v149 src0_sel:WORD_1
	s_nop 0
	v_pk_fma_f32 v[172:173], v[188:189], s[6:7], v[172:173] op_sel_hi:[1,0,1]
	v_pk_fma_f32 v[174:175], v[190:191], s[6:7], v[174:175] op_sel_hi:[1,0,1]
	v_cvt_pk_f32_fp8_e32 v[184:185], v150
	v_cvt_pk_f32_fp8_sdwa v[186:187], v150 src0_sel:WORD_1
	s_nop 0
	v_pk_fma_f32 v[176:177], v[184:185], s[6:7], v[176:177] op_sel_hi:[1,0,1]
	v_pk_fma_f32 v[178:179], v[186:187], s[6:7], v[178:179] op_sel_hi:[1,0,1]
	v_cvt_pk_f32_fp8_e32 v[188:189], v151
	v_cvt_pk_f32_fp8_sdwa v[190:191], v151 src0_sel:WORD_1
	s_nop 0
	v_pk_fma_f32 v[180:181], v[188:189], s[6:7], v[180:181] op_sel_hi:[1,0,1]
	v_pk_fma_f32 v[182:183], v[190:191], s[6:7], v[182:183] op_sel_hi:[1,0,1]
.Lcb_s3_1:
	s_bitcmp1_b32 s10, 2
	s_cbranch_scc0 .Lcb_s3_2
	v_cvt_pk_f32_fp8_e32 v[184:185], v152
	v_cvt_pk_f32_fp8_sdwa v[186:187], v152 src0_sel:WORD_1
	s_nop 0
	v_pk_fma_f32 v[168:169], v[184:185], s[6:7], v[168:169] op_sel_hi:[1,0,1]
	v_pk_fma_f32 v[170:171], v[186:187], s[6:7], v[170:171] op_sel_hi:[1,0,1]
	v_cvt_pk_f32_fp8_e32 v[188:189], v153
	v_cvt_pk_f32_fp8_sdwa v[190:191], v153 src0_sel:WORD_1
	s_nop 0
	v_pk_fma_f32 v[172:173], v[188:189], s[6:7], v[172:173] op_sel_hi:[1,0,1]
	v_pk_fma_f32 v[174:175], v[190:191], s[6:7], v[174:175] op_sel_hi:[1,0,1]
	v_cvt_pk_f32_fp8_e32 v[184:185], v154
	v_cvt_pk_f32_fp8_sdwa v[186:187], v154 src0_sel:WORD_1
	s_nop 0
	v_pk_fma_f32 v[176:177], v[184:185], s[6:7], v[176:177] op_sel_hi:[1,0,1]
	v_pk_fma_f32 v[178:179], v[186:187], s[6:7], v[178:179] op_sel_hi:[1,0,1]
	v_cvt_pk_f32_fp8_e32 v[188:189], v155
	v_cvt_pk_f32_fp8_sdwa v[190:191], v155 src0_sel:WORD_1
	s_nop 0
	v_pk_fma_f32 v[180:181], v[188:189], s[6:7], v[180:181] op_sel_hi:[1,0,1]
	v_pk_fma_f32 v[182:183], v[190:191], s[6:7], v[182:183] op_sel_hi:[1,0,1]
.Lcb_s3_2:
	s_bitcmp1_b32 s10, 3
	s_cbranch_scc0 .Lcb_s3_3
	v_cvt_pk_f32_fp8_e32 v[184:185], v156
	v_cvt_pk_f32_fp8_sdwa v[186:187], v156 src0_sel:WORD_1
	s_nop 0
	v_pk_fma_f32 v[168:169], v[184:185], s[6:7], v[168:169] op_sel_hi:[1,0,1]
	v_pk_fma_f32 v[170:171], v[186:187], s[6:7], v[170:171] op_sel_hi:[1,0,1]
	v_cvt_pk_f32_fp8_e32 v[188:189], v157
	v_cvt_pk_f32_fp8_sdwa v[190:191], v157 src0_sel:WORD_1
	s_nop 0
	v_pk_fma_f32 v[172:173], v[188:189], s[6:7], v[172:173] op_sel_hi:[1,0,1]
	v_pk_fma_f32 v[174:175], v[190:191], s[6:7], v[174:175] op_sel_hi:[1,0,1]
	v_cvt_pk_f32_fp8_e32 v[184:185], v158
	v_cvt_pk_f32_fp8_sdwa v[186:187], v158 src0_sel:WORD_1
	s_nop 0
	v_pk_fma_f32 v[176:177], v[184:185], s[6:7], v[176:177] op_sel_hi:[1,0,1]
	v_pk_fma_f32 v[178:179], v[186:187], s[6:7], v[178:179] op_sel_hi:[1,0,1]
	v_cvt_pk_f32_fp8_e32 v[188:189], v159
	v_cvt_pk_f32_fp8_sdwa v[190:191], v159 src0_sel:WORD_1
	s_nop 0
	v_pk_fma_f32 v[180:181], v[188:189], s[6:7], v[180:181] op_sel_hi:[1,0,1]
	v_pk_fma_f32 v[182:183], v[190:191], s[6:7], v[182:183] op_sel_hi:[1,0,1]
.Lcb_s3_3:
	s_bitcmp1_b32 s10, 4
	s_cbranch_scc0 .Lcb_s3_4
	v_cvt_pk_f32_fp8_e32 v[184:185], v160
	v_cvt_pk_f32_fp8_sdwa v[186:187], v160 src0_sel:WORD_1
	s_nop 0
	v_pk_fma_f32 v[168:169], v[184:185], s[6:7], v[168:169] op_sel_hi:[1,0,1]
	v_pk_fma_f32 v[170:171], v[186:187], s[6:7], v[170:171] op_sel_hi:[1,0,1]
	v_cvt_pk_f32_fp8_e32 v[188:189], v161
	v_cvt_pk_f32_fp8_sdwa v[190:191], v161 src0_sel:WORD_1
	s_nop 0
	v_pk_fma_f32 v[172:173], v[188:189], s[6:7], v[172:173] op_sel_hi:[1,0,1]
	v_pk_fma_f32 v[174:175], v[190:191], s[6:7], v[174:175] op_sel_hi:[1,0,1]
	v_cvt_pk_f32_fp8_e32 v[184:185], v162
	v_cvt_pk_f32_fp8_sdwa v[186:187], v162 src0_sel:WORD_1
	s_nop 0
	v_pk_fma_f32 v[176:177], v[184:185], s[6:7], v[176:177] op_sel_hi:[1,0,1]
	v_pk_fma_f32 v[178:179], v[186:187], s[6:7], v[178:179] op_sel_hi:[1,0,1]
	v_cvt_pk_f32_fp8_e32 v[188:189], v163
	v_cvt_pk_f32_fp8_sdwa v[190:191], v163 src0_sel:WORD_1
	s_nop 0
	v_pk_fma_f32 v[180:181], v[188:189], s[6:7], v[180:181] op_sel_hi:[1,0,1]
	v_pk_fma_f32 v[182:183], v[190:191], s[6:7], v[182:183] op_sel_hi:[1,0,1]
.Lcb_s3_4:
	s_bitcmp1_b32 s10, 5
	s_cbranch_scc0 .Lcb_s3_5
	v_cvt_pk_f32_fp8_e32 v[184:185], v164
	v_cvt_pk_f32_fp8_sdwa v[186:187], v164 src0_sel:WORD_1
	s_nop 0
	v_pk_fma_f32 v[168:169], v[184:185], s[6:7], v[168:169] op_sel_hi:[1,0,1]
	v_pk_fma_f32 v[170:171], v[186:187], s[6:7], v[170:171] op_sel_hi:[1,0,1]
	v_cvt_pk_f32_fp8_e32 v[188:189], v165
	v_cvt_pk_f32_fp8_sdwa v[190:191], v165 src0_sel:WORD_1
	s_nop 0
	v_pk_fma_f32 v[172:173], v[188:189], s[6:7], v[172:173] op_sel_hi:[1,0,1]
	v_pk_fma_f32 v[174:175], v[190:191], s[6:7], v[174:175] op_sel_hi:[1,0,1]
	v_cvt_pk_f32_fp8_e32 v[184:185], v166
	v_cvt_pk_f32_fp8_sdwa v[186:187], v166 src0_sel:WORD_1
	s_nop 0
	v_pk_fma_f32 v[176:177], v[184:185], s[6:7], v[176:177] op_sel_hi:[1,0,1]
	v_pk_fma_f32 v[178:179], v[186:187], s[6:7], v[178:179] op_sel_hi:[1,0,1]
	v_cvt_pk_f32_fp8_e32 v[188:189], v167
	v_cvt_pk_f32_fp8_sdwa v[190:191], v167 src0_sel:WORD_1
	s_nop 0
	v_pk_fma_f32 v[180:181], v[188:189], s[6:7], v[180:181] op_sel_hi:[1,0,1]
	v_pk_fma_f32 v[182:183], v[190:191], s[6:7], v[182:183] op_sel_hi:[1,0,1]

.Lcb_ov3:
	s_ff1_i32_b32 s26, s9
	s_add_i32 s27, s9, -1
	v_readlane_b32 s26, v69, s26
	s_and_b32 s9, s9, s27
	s_lshl_b32 s26, s26, 10
	s_add_u32 s26, s4, s26
	s_addc_u32 s27, s5, 0
	global_load_dwordx4 v[200:203], v212, s[26:27] nt
	s_waitcnt vmcnt(0)
	v_cvt_pk_f32_fp8_e32 v[184:185], v200
	v_cvt_pk_f32_fp8_sdwa v[186:187], v200 src0_sel:WORD_1
	s_nop 0
	v_pk_fma_f32 v[168:169], v[184:185], s[6:7], v[168:169] op_sel_hi:[1,0,1]
	v_pk_fma_f32 v[170:171], v[186:187], s[6:7], v[170:171] op_sel_hi:[1,0,1]
	v_cvt_pk_f32_fp8_e32 v[188:189], v201
	v_cvt_pk_f32_fp8_sdwa v[190:191], v201 src0_sel:WORD_1
	s_nop 0
	v_pk_fma_f32 v[172:173], v[188:189], s[6:7], v[172:173] op_sel_hi:[1,0,1]
	v_pk_fma_f32 v[174:175], v[190:191], s[6:7], v[174:175] op_sel_hi:[1,0,1]
	v_cvt_pk_f32_fp8_e32 v[184:185], v202
	v_cvt_pk_f32_fp8_sdwa v[186:187], v202 src0_sel:WORD_1
	s_nop 0
	v_pk_fma_f32 v[176:177], v[184:185], s[6:7], v[176:177] op_sel_hi:[1,0,1]
	v_pk_fma_f32 v[178:179], v[186:187], s[6:7], v[178:179] op_sel_hi:[1,0,1]
	v_cvt_pk_f32_fp8_e32 v[188:189], v203
	v_cvt_pk_f32_fp8_sdwa v[190:191], v203 src0_sel:WORD_1
	s_nop 0
	v_pk_fma_f32 v[180:181], v[188:189], s[6:7], v[180:181] op_sel_hi:[1,0,1]
	v_pk_fma_f32 v[182:183], v[190:191], s[6:7], v[182:183] op_sel_hi:[1,0,1]
	s_cmp_lg_u32 s9, 0
	s_cbranch_scc1 .Lcb_ov3
.Lcb_ov_done3:
	s_add_i32 s9, s8, 0x1800
	s_cmp_eq_u32 s52, 3
	s_cbranch_scc0 .Lcb_mid3
	s_lshl_b32 s10, s9, 12
	s_add_u32 s12, s14, s10
	s_addc_u32 s13, s15, 0
	global_store_dwordx4 v214, v[168:171], s[12:13]
	global_store_dwordx4 v214, v[172:175], s[12:13] offset:16
	global_store_dwordx4 v214, v[176:179], s[12:13] offset:32
	global_store_dwordx4 v214, v[180:183], s[12:13] offset:48
	s_branch .Lcb_done3

.Lcb_done3:
	s_add_i32 s9, s8, 0x4800
	s_lshr_b32 s10, s9, 12
	s_lshl_b32 s10, s10, 18
	s_and_b32 s12, s9, 0xfff
	s_lshl_b32 s12, s12, 2
	s_add_i32 s10, s10, s12
	s_add_u32 s12, s0, 0x37b00000
	s_addc_u32 s13, s1, 0
	s_add_u32 s12, s12, s10
	s_addc_u32 s13, s13, 0
	global_load_dword v69, v215, s[12:13]
	s_lshl_b32 s10, s9, 11
	s_add_u32 s12, s0, 0x37e00000
	s_addc_u32 s13, s1, 0
	s_add_u32 s12, s12, s10
	s_addc_u32 s13, s13, 0
	global_load_dwordx4 v[42:45], v213, s[12:13] nt
	global_load_dwordx4 v[46:49], v213, s[12:13] offset:16 nt
	s_waitcnt vmcnt(26)
	v_cmp_le_i32_e64 s[24:25], 0, v67
	s_mov_b32 s10, 0
	s_and_b32 s9, s24, 0xffff
	s_cmp_lg_u32 s9, 0
	s_cbranch_scc0 .Lcb_n7_0
	s_ff1_i32_b32 s26, s9
	s_add_i32 s27, s9, -1
	v_readlane_b32 s26, v67, s26
	s_and_b32 s9, s9, s27
	s_bitset1_b32 s10, 0
	s_lshl_b32 s26, s26, 10
	s_add_u32 s26, s4, s26
	s_addc_u32 s27, s5, 0
	s_branch .Lcb_l7_0

.Lcb_l7_0:
	global_load_dwordx4 v[144:147], v212, s[26:27] nt
	s_cmp_lg_u32 s9, 0
	s_cbranch_scc0 .Lcb_n7_1
	s_ff1_i32_b32 s26, s9
	s_add_i32 s27, s9, -1
	v_readlane_b32 s26, v67, s26
	s_and_b32 s9, s9, s27
	s_bitset1_b32 s10, 1
	s_lshl_b32 s26, s26, 10
	s_add_u32 s26, s4, s26
	s_addc_u32 s27, s5, 0
	s_branch .Lcb_l7_1

.Lcb_l7_1:
	global_load_dwordx4 v[148:151], v212, s[26:27] nt
	s_cmp_lg_u32 s9, 0
	s_cbranch_scc0 .Lcb_n7_2
	s_ff1_i32_b32 s26, s9
	s_add_i32 s27, s9, -1
	v_readlane_b32 s26, v67, s26
	s_and_b32 s9, s9, s27
	s_bitset1_b32 s10, 2
	s_lshl_b32 s26, s26, 10
	s_add_u32 s26, s4, s26
	s_addc_u32 s27, s5, 0
	s_branch .Lcb_l7_2

.Lcb_l7_2:
	global_load_dwordx4 v[152:155], v212, s[26:27] nt
	s_cmp_lg_u32 s9, 0
	s_cbranch_scc0 .Lcb_n7_3
	s_ff1_i32_b32 s26, s9
	s_add_i32 s27, s9, -1
	v_readlane_b32 s26, v67, s26
	s_and_b32 s9, s9, s27
	s_bitset1_b32 s10, 3
	s_lshl_b32 s26, s26, 10
	s_add_u32 s26, s4, s26
	s_addc_u32 s27, s5, 0
	s_branch .Lcb_l7_3

.Lcb_l7_3:
	global_load_dwordx4 v[156:159], v212, s[26:27] nt
	s_cmp_lg_u32 s9, 0
	s_cbranch_scc0 .Lcb_n7_4
	s_ff1_i32_b32 s26, s9
	s_add_i32 s27, s9, -1
	v_readlane_b32 s26, v67, s26
	s_and_b32 s9, s9, s27
	s_bitset1_b32 s10, 4
	s_lshl_b32 s26, s26, 10
	s_add_u32 s26, s4, s26
	s_addc_u32 s27, s5, 0
	s_branch .Lcb_l7_4

.Lcb_l7_4:
	global_load_dwordx4 v[160:163], v212, s[26:27] nt
	s_cmp_lg_u32 s9, 0
	s_cbranch_scc0 .Lcb_n7_5
	s_ff1_i32_b32 s26, s9
	s_add_i32 s27, s9, -1
	v_readlane_b32 s26, v67, s26
	s_and_b32 s9, s9, s27
	s_bitset1_b32 s10, 5
	s_lshl_b32 s26, s26, 10
	s_add_u32 s26, s4, s26
	s_addc_u32 s27, s5, 0
	s_branch .Lcb_l7_5

.Lcb_l7_5:
	global_load_dwordx4 v[164:167], v212, s[26:27] nt
	v_writelane_b32 v210, s10, 7
	v_writelane_b32 v211, s9, 7
	s_waitcnt vmcnt(39)
	v_lshlrev_b32_e32 v168, 16, v50
	v_and_b32_e32 v169, 0xffff0000, v50
	v_lshlrev_b32_e32 v170, 16, v51
	v_and_b32_e32 v171, 0xffff0000, v51
	v_lshlrev_b32_e32 v172, 16, v52
	v_and_b32_e32 v173, 0xffff0000, v52
	v_lshlrev_b32_e32 v174, 16, v53
	v_and_b32_e32 v175, 0xffff0000, v53
	v_lshlrev_b32_e32 v176, 16, v54
	v_and_b32_e32 v177, 0xffff0000, v54
	v_lshlrev_b32_e32 v178, 16, v55
	v_and_b32_e32 v179, 0xffff0000, v55
	v_lshlrev_b32_e32 v180, 16, v56
	v_and_b32_e32 v181, 0xffff0000, v56
	v_lshlrev_b32_e32 v182, 16, v57
	v_and_b32_e32 v183, 0xffff0000, v57
	v_readlane_b32 s10, v210, 4
	v_readlane_b32 s9, v211, 4
	s_bitcmp1_b32 s10, 0
	s_cbranch_scc0 .Lcb_s4_0
	v_cvt_pk_f32_fp8_e32 v[184:185], v72
	v_cvt_pk_f32_fp8_sdwa v[186:187], v72 src0_sel:WORD_1
	s_nop 0
	v_pk_fma_f32 v[168:169], v[184:185], s[6:7], v[168:169] op_sel_hi:[1,0,1]
	v_pk_fma_f32 v[170:171], v[186:187], s[6:7], v[170:171] op_sel_hi:[1,0,1]
	v_cvt_pk_f32_fp8_e32 v[188:189], v73
	v_cvt_pk_f32_fp8_sdwa v[190:191], v73 src0_sel:WORD_1
	s_nop 0
	v_pk_fma_f32 v[172:173], v[188:189], s[6:7], v[172:173] op_sel_hi:[1,0,1]
	v_pk_fma_f32 v[174:175], v[190:191], s[6:7], v[174:175] op_sel_hi:[1,0,1]
	v_cvt_pk_f32_fp8_e32 v[184:185], v74
	v_cvt_pk_f32_fp8_sdwa v[186:187], v74 src0_sel:WORD_1
	s_nop 0
	v_pk_fma_f32 v[176:177], v[184:185], s[6:7], v[176:177] op_sel_hi:[1,0,1]
	v_pk_fma_f32 v[178:179], v[186:187], s[6:7], v[178:179] op_sel_hi:[1,0,1]
	v_cvt_pk_f32_fp8_e32 v[188:189], v75
	v_cvt_pk_f32_fp8_sdwa v[190:191], v75 src0_sel:WORD_1
	s_nop 0
	v_pk_fma_f32 v[180:181], v[188:189], s[6:7], v[180:181] op_sel_hi:[1,0,1]
	v_pk_fma_f32 v[182:183], v[190:191], s[6:7], v[182:183] op_sel_hi:[1,0,1]

.Lcb_ov4:
	s_ff1_i32_b32 s26, s9
	s_add_i32 s27, s9, -1
	v_readlane_b32 s26, v70, s26
	s_and_b32 s9, s9, s27
	s_lshl_b32 s26, s26, 10
	s_add_u32 s26, s4, s26
	s_addc_u32 s27, s5, 0
	global_load_dwordx4 v[200:203], v212, s[26:27] nt
	s_waitcnt vmcnt(0)
	v_cvt_pk_f32_fp8_e32 v[184:185], v200
	v_cvt_pk_f32_fp8_sdwa v[186:187], v200 src0_sel:WORD_1
	s_nop 0
	v_pk_fma_f32 v[168:169], v[184:185], s[6:7], v[168:169] op_sel_hi:[1,0,1]
	v_pk_fma_f32 v[170:171], v[186:187], s[6:7], v[170:171] op_sel_hi:[1,0,1]
	v_cvt_pk_f32_fp8_e32 v[188:189], v201
	v_cvt_pk_f32_fp8_sdwa v[190:191], v201 src0_sel:WORD_1
	s_nop 0
	v_pk_fma_f32 v[172:173], v[188:189], s[6:7], v[172:173] op_sel_hi:[1,0,1]
	v_pk_fma_f32 v[174:175], v[190:191], s[6:7], v[174:175] op_sel_hi:[1,0,1]
	v_cvt_pk_f32_fp8_e32 v[184:185], v202
	v_cvt_pk_f32_fp8_sdwa v[186:187], v202 src0_sel:WORD_1
	s_nop 0
	v_pk_fma_f32 v[176:177], v[184:185], s[6:7], v[176:177] op_sel_hi:[1,0,1]
	v_pk_fma_f32 v[178:179], v[186:187], s[6:7], v[178:179] op_sel_hi:[1,0,1]
	v_cvt_pk_f32_fp8_e32 v[188:189], v203
	v_cvt_pk_f32_fp8_sdwa v[190:191], v203 src0_sel:WORD_1
	s_nop 0
	v_pk_fma_f32 v[180:181], v[188:189], s[6:7], v[180:181] op_sel_hi:[1,0,1]
	v_pk_fma_f32 v[182:183], v[190:191], s[6:7], v[182:183] op_sel_hi:[1,0,1]
	s_cmp_lg_u32 s9, 0
	s_cbranch_scc1 .Lcb_ov4
.Lcb_ov_done4:
	s_add_i32 s9, s8, 0x2000
	s_cmp_eq_u32 s52, 3
	s_cbranch_scc0 .Lcb_mid4
	s_lshl_b32 s10, s9, 12
	s_add_u32 s12, s14, s10
	s_addc_u32 s13, s15, 0
	global_store_dwordx4 v214, v[168:171], s[12:13]
	global_store_dwordx4 v214, v[172:175], s[12:13] offset:16
	global_store_dwordx4 v214, v[176:179], s[12:13] offset:32
	global_store_dwordx4 v214, v[180:183], s[12:13] offset:48
	s_branch .Lcb_done4

.Lcb_done4:
	s_add_i32 s9, s8, 0x5000
	s_lshr_b32 s10, s9, 12
	s_lshl_b32 s10, s10, 18
	s_and_b32 s12, s9, 0xfff
	s_lshl_b32 s12, s12, 2
	s_add_i32 s10, s10, s12
	s_add_u32 s12, s0, 0x37b00000
	s_addc_u32 s13, s1, 0
	s_add_u32 s12, s12, s10
	s_addc_u32 s13, s13, 0
	global_load_dword v70, v215, s[12:13]
	s_lshl_b32 s10, s9, 11
	s_add_u32 s12, s0, 0x37e00000
	s_addc_u32 s13, s1, 0
	s_add_u32 s12, s12, s10
	s_addc_u32 s13, s13, 0
	global_load_dwordx4 v[50:53], v213, s[12:13] nt
	global_load_dwordx4 v[54:57], v213, s[12:13] offset:16 nt
	s_waitcnt vmcnt(26)
	v_cmp_le_i32_e64 s[24:25], 0, v68
	s_mov_b32 s10, 0
	s_and_b32 s9, s24, 0xffff
	s_cmp_lg_u32 s9, 0
	s_cbranch_scc0 .Lcb_n8_0
	s_ff1_i32_b32 s26, s9
	s_add_i32 s27, s9, -1
	v_readlane_b32 s26, v68, s26
	s_and_b32 s9, s9, s27
	s_bitset1_b32 s10, 0
	s_lshl_b32 s26, s26, 10
	s_add_u32 s26, s4, s26
	s_addc_u32 s27, s5, 0
	s_branch .Lcb_l8_0

.Lcb_l8_0:
	global_load_dwordx4 v[72:75], v212, s[26:27] nt
	s_cmp_lg_u32 s9, 0
	s_cbranch_scc0 .Lcb_n8_1
	s_ff1_i32_b32 s26, s9
	s_add_i32 s27, s9, -1
	v_readlane_b32 s26, v68, s26
	s_and_b32 s9, s9, s27
	s_bitset1_b32 s10, 1
	s_lshl_b32 s26, s26, 10
	s_add_u32 s26, s4, s26
	s_addc_u32 s27, s5, 0
	s_branch .Lcb_l8_1

.Lcb_l8_1:
	global_load_dwordx4 v[76:79], v212, s[26:27] nt
	s_cmp_lg_u32 s9, 0
	s_cbranch_scc0 .Lcb_n8_2
	s_ff1_i32_b32 s26, s9
	s_add_i32 s27, s9, -1
	v_readlane_b32 s26, v68, s26
	s_and_b32 s9, s9, s27
	s_bitset1_b32 s10, 2
	s_lshl_b32 s26, s26, 10
	s_add_u32 s26, s4, s26
	s_addc_u32 s27, s5, 0
	s_branch .Lcb_l8_2

.Lcb_l8_2:
	global_load_dwordx4 v[80:83], v212, s[26:27] nt
	s_cmp_lg_u32 s9, 0
	s_cbranch_scc0 .Lcb_n8_3
	s_ff1_i32_b32 s26, s9
	s_add_i32 s27, s9, -1
	v_readlane_b32 s26, v68, s26
	s_and_b32 s9, s9, s27
	s_bitset1_b32 s10, 3
	s_lshl_b32 s26, s26, 10
	s_add_u32 s26, s4, s26
	s_addc_u32 s27, s5, 0
	s_branch .Lcb_l8_3

.Lcb_l8_3:
	global_load_dwordx4 v[84:87], v212, s[26:27] nt
	s_cmp_lg_u32 s9, 0
	s_cbranch_scc0 .Lcb_n8_4
	s_ff1_i32_b32 s26, s9
	s_add_i32 s27, s9, -1
	v_readlane_b32 s26, v68, s26
	s_and_b32 s9, s9, s27
	s_bitset1_b32 s10, 4
	s_lshl_b32 s26, s26, 10
	s_add_u32 s26, s4, s26
	s_addc_u32 s27, s5, 0
	s_branch .Lcb_l8_4

.Lcb_l8_4:
	global_load_dwordx4 v[88:91], v212, s[26:27] nt
	s_cmp_lg_u32 s9, 0
	s_cbranch_scc0 .Lcb_n8_5
	s_ff1_i32_b32 s26, s9
	s_add_i32 s27, s9, -1
	v_readlane_b32 s26, v68, s26
	s_and_b32 s9, s9, s27
	s_bitset1_b32 s10, 5
	s_lshl_b32 s26, s26, 10
	s_add_u32 s26, s4, s26
	s_addc_u32 s27, s5, 0
	s_branch .Lcb_l8_5

.Lcb_l8_5:
	global_load_dwordx4 v[92:95], v212, s[26:27] nt
	v_writelane_b32 v210, s10, 8
	v_writelane_b32 v211, s9, 8
	s_waitcnt vmcnt(39)
	v_lshlrev_b32_e32 v168, 16, v58
	v_and_b32_e32 v169, 0xffff0000, v58
	v_lshlrev_b32_e32 v170, 16, v59
	v_and_b32_e32 v171, 0xffff0000, v59
	v_lshlrev_b32_e32 v172, 16, v60
	v_and_b32_e32 v173, 0xffff0000, v60
	v_lshlrev_b32_e32 v174, 16, v61
	v_and_b32_e32 v175, 0xffff0000, v61
	v_lshlrev_b32_e32 v176, 16, v62
	v_and_b32_e32 v177, 0xffff0000, v62
	v_lshlrev_b32_e32 v178, 16, v63
	v_and_b32_e32 v179, 0xffff0000, v63
	v_lshlrev_b32_e32 v180, 16, v64
	v_and_b32_e32 v181, 0xffff0000, v64
	v_lshlrev_b32_e32 v182, 16, v65
	v_and_b32_e32 v183, 0xffff0000, v65
	v_readlane_b32 s10, v210, 5
	v_readlane_b32 s9, v211, 5
	s_bitcmp1_b32 s10, 0
	s_cbranch_scc0 .Lcb_s5_0
	v_cvt_pk_f32_fp8_e32 v[184:185], v96
	v_cvt_pk_f32_fp8_sdwa v[186:187], v96 src0_sel:WORD_1
	s_nop 0
	v_pk_fma_f32 v[168:169], v[184:185], s[6:7], v[168:169] op_sel_hi:[1,0,1]
	v_pk_fma_f32 v[170:171], v[186:187], s[6:7], v[170:171] op_sel_hi:[1,0,1]
	v_cvt_pk_f32_fp8_e32 v[188:189], v97
	v_cvt_pk_f32_fp8_sdwa v[190:191], v97 src0_sel:WORD_1
	s_nop 0
	v_pk_fma_f32 v[172:173], v[188:189], s[6:7], v[172:173] op_sel_hi:[1,0,1]
	v_pk_fma_f32 v[174:175], v[190:191], s[6:7], v[174:175] op_sel_hi:[1,0,1]
	v_cvt_pk_f32_fp8_e32 v[184:185], v98
	v_cvt_pk_f32_fp8_sdwa v[186:187], v98 src0_sel:WORD_1
	s_nop 0
	v_pk_fma_f32 v[176:177], v[184:185], s[6:7], v[176:177] op_sel_hi:[1,0,1]
	v_pk_fma_f32 v[178:179], v[186:187], s[6:7], v[178:179] op_sel_hi:[1,0,1]
	v_cvt_pk_f32_fp8_e32 v[188:189], v99
	v_cvt_pk_f32_fp8_sdwa v[190:191], v99 src0_sel:WORD_1
	s_nop 0
	v_pk_fma_f32 v[180:181], v[188:189], s[6:7], v[180:181] op_sel_hi:[1,0,1]
	v_pk_fma_f32 v[182:183], v[190:191], s[6:7], v[182:183] op_sel_hi:[1,0,1]

.Lcb_ov5:
	s_ff1_i32_b32 s26, s9
	s_add_i32 s27, s9, -1
	v_readlane_b32 s26, v71, s26
	s_and_b32 s9, s9, s27
	s_lshl_b32 s26, s26, 10
	s_add_u32 s26, s4, s26
	s_addc_u32 s27, s5, 0
	global_load_dwordx4 v[200:203], v212, s[26:27] nt
	s_waitcnt vmcnt(0)
	v_cvt_pk_f32_fp8_e32 v[184:185], v200
	v_cvt_pk_f32_fp8_sdwa v[186:187], v200 src0_sel:WORD_1
	s_nop 0
	v_pk_fma_f32 v[168:169], v[184:185], s[6:7], v[168:169] op_sel_hi:[1,0,1]
	v_pk_fma_f32 v[170:171], v[186:187], s[6:7], v[170:171] op_sel_hi:[1,0,1]
	v_cvt_pk_f32_fp8_e32 v[188:189], v201
	v_cvt_pk_f32_fp8_sdwa v[190:191], v201 src0_sel:WORD_1
	s_nop 0
	v_pk_fma_f32 v[172:173], v[188:189], s[6:7], v[172:173] op_sel_hi:[1,0,1]
	v_pk_fma_f32 v[174:175], v[190:191], s[6:7], v[174:175] op_sel_hi:[1,0,1]
	v_cvt_pk_f32_fp8_e32 v[184:185], v202
	v_cvt_pk_f32_fp8_sdwa v[186:187], v202 src0_sel:WORD_1
	s_nop 0
	v_pk_fma_f32 v[176:177], v[184:185], s[6:7], v[176:177] op_sel_hi:[1,0,1]
	v_pk_fma_f32 v[178:179], v[186:187], s[6:7], v[178:179] op_sel_hi:[1,0,1]
	v_cvt_pk_f32_fp8_e32 v[188:189], v203
	v_cvt_pk_f32_fp8_sdwa v[190:191], v203 src0_sel:WORD_1
	s_nop 0
	v_pk_fma_f32 v[180:181], v[188:189], s[6:7], v[180:181] op_sel_hi:[1,0,1]
	v_pk_fma_f32 v[182:183], v[190:191], s[6:7], v[182:183] op_sel_hi:[1,0,1]
	s_cmp_lg_u32 s9, 0
	s_cbranch_scc1 .Lcb_ov5
.Lcb_ov_done5:
	s_add_i32 s9, s8, 0x2800
	s_cmp_eq_u32 s52, 3
	s_cbranch_scc0 .Lcb_mid5
	s_lshl_b32 s10, s9, 12
	s_add_u32 s12, s14, s10
	s_addc_u32 s13, s15, 0
	global_store_dwordx4 v214, v[168:171], s[12:13]
	global_store_dwordx4 v214, v[172:175], s[12:13] offset:16
	global_store_dwordx4 v214, v[176:179], s[12:13] offset:32
	global_store_dwordx4 v214, v[180:183], s[12:13] offset:48
	s_branch .Lcb_done5

.Lcb_done5:
	s_add_i32 s9, s8, 0x5800
	s_lshr_b32 s10, s9, 12
	s_lshl_b32 s10, s10, 18
	s_and_b32 s12, s9, 0xfff
	s_lshl_b32 s12, s12, 2
	s_add_i32 s10, s10, s12
	s_add_u32 s12, s0, 0x37b00000
	s_addc_u32 s13, s1, 0
	s_add_u32 s12, s12, s10
	s_addc_u32 s13, s13, 0
	global_load_dword v71, v215, s[12:13]
	s_lshl_b32 s10, s9, 11
	s_add_u32 s12, s0, 0x37e00000
	s_addc_u32 s13, s1, 0
	s_add_u32 s12, s12, s10
	s_addc_u32 s13, s13, 0
	global_load_dwordx4 v[58:61], v213, s[12:13] nt
	global_load_dwordx4 v[62:65], v213, s[12:13] offset:16 nt
	s_waitcnt vmcnt(26)
	v_cmp_le_i32_e64 s[24:25], 0, v69
	s_mov_b32 s10, 0
	s_and_b32 s9, s24, 0xffff
	s_cmp_lg_u32 s9, 0
	s_cbranch_scc0 .Lcb_n9_0
	s_ff1_i32_b32 s26, s9
	s_add_i32 s27, s9, -1
	v_readlane_b32 s26, v69, s26
	s_and_b32 s9, s9, s27
	s_bitset1_b32 s10, 0
	s_lshl_b32 s26, s26, 10
	s_add_u32 s26, s4, s26
	s_addc_u32 s27, s5, 0
	s_branch .Lcb_l9_0

.Lcb_l9_0:
	global_load_dwordx4 v[96:99], v212, s[26:27] nt
	s_cmp_lg_u32 s9, 0
	s_cbranch_scc0 .Lcb_n9_1
	s_ff1_i32_b32 s26, s9
	s_add_i32 s27, s9, -1
	v_readlane_b32 s26, v69, s26
	s_and_b32 s9, s9, s27
	s_bitset1_b32 s10, 1
	s_lshl_b32 s26, s26, 10
	s_add_u32 s26, s4, s26
	s_addc_u32 s27, s5, 0
	s_branch .Lcb_l9_1

.Lcb_l9_1:
	global_load_dwordx4 v[100:103], v212, s[26:27] nt
	s_cmp_lg_u32 s9, 0
	s_cbranch_scc0 .Lcb_n9_2
	s_ff1_i32_b32 s26, s9
	s_add_i32 s27, s9, -1
	v_readlane_b32 s26, v69, s26
	s_and_b32 s9, s9, s27
	s_bitset1_b32 s10, 2
	s_lshl_b32 s26, s26, 10
	s_add_u32 s26, s4, s26
	s_addc_u32 s27, s5, 0
	s_branch .Lcb_l9_2

.Lcb_l9_2:
	global_load_dwordx4 v[104:107], v212, s[26:27] nt
	s_cmp_lg_u32 s9, 0
	s_cbranch_scc0 .Lcb_n9_3
	s_ff1_i32_b32 s26, s9
	s_add_i32 s27, s9, -1
	v_readlane_b32 s26, v69, s26
	s_and_b32 s9, s9, s27
	s_bitset1_b32 s10, 3
	s_lshl_b32 s26, s26, 10
	s_add_u32 s26, s4, s26
	s_addc_u32 s27, s5, 0
	s_branch .Lcb_l9_3

.Lcb_l9_3:
	global_load_dwordx4 v[108:111], v212, s[26:27] nt
	s_cmp_lg_u32 s9, 0
	s_cbranch_scc0 .Lcb_n9_4
	s_ff1_i32_b32 s26, s9
	s_add_i32 s27, s9, -1
	v_readlane_b32 s26, v69, s26
	s_and_b32 s9, s9, s27
	s_bitset1_b32 s10, 4
	s_lshl_b32 s26, s26, 10
	s_add_u32 s26, s4, s26
	s_addc_u32 s27, s5, 0
	s_branch .Lcb_l9_4

.Lcb_l9_4:
	global_load_dwordx4 v[112:115], v212, s[26:27] nt
	s_cmp_lg_u32 s9, 0
	s_cbranch_scc0 .Lcb_n9_5
	s_ff1_i32_b32 s26, s9
	s_add_i32 s27, s9, -1
	v_readlane_b32 s26, v69, s26
	s_and_b32 s9, s9, s27
	s_bitset1_b32 s10, 5
	s_lshl_b32 s26, s26, 10
	s_add_u32 s26, s4, s26
	s_addc_u32 s27, s5, 0
	s_branch .Lcb_l9_5

.Lcb_l9_5:
	global_load_dwordx4 v[116:119], v212, s[26:27] nt
	v_writelane_b32 v210, s10, 9
	v_writelane_b32 v211, s9, 9
	s_waitcnt vmcnt(39)
	v_lshlrev_b32_e32 v168, 16, v18
	v_and_b32_e32 v169, 0xffff0000, v18
	v_lshlrev_b32_e32 v170, 16, v19
	v_and_b32_e32 v171, 0xffff0000, v19
	v_lshlrev_b32_e32 v172, 16, v20
	v_and_b32_e32 v173, 0xffff0000, v20
	v_lshlrev_b32_e32 v174, 16, v21
	v_and_b32_e32 v175, 0xffff0000, v21
	v_lshlrev_b32_e32 v176, 16, v22
	v_and_b32_e32 v177, 0xffff0000, v22
	v_lshlrev_b32_e32 v178, 16, v23
	v_and_b32_e32 v179, 0xffff0000, v23
	v_lshlrev_b32_e32 v180, 16, v24
	v_and_b32_e32 v181, 0xffff0000, v24
	v_lshlrev_b32_e32 v182, 16, v25
	v_and_b32_e32 v183, 0xffff0000, v25
	v_readlane_b32 s10, v210, 6
	v_readlane_b32 s9, v211, 6
	s_bitcmp1_b32 s10, 0
	s_cbranch_scc0 .Lcb_s6_0
	v_cvt_pk_f32_fp8_e32 v[184:185], v120
	v_cvt_pk_f32_fp8_sdwa v[186:187], v120 src0_sel:WORD_1
	s_nop 0
	v_pk_fma_f32 v[168:169], v[184:185], s[6:7], v[168:169] op_sel_hi:[1,0,1]
	v_pk_fma_f32 v[170:171], v[186:187], s[6:7], v[170:171] op_sel_hi:[1,0,1]
	v_cvt_pk_f32_fp8_e32 v[188:189], v121
	v_cvt_pk_f32_fp8_sdwa v[190:191], v121 src0_sel:WORD_1
	s_nop 0
	v_pk_fma_f32 v[172:173], v[188:189], s[6:7], v[172:173] op_sel_hi:[1,0,1]
	v_pk_fma_f32 v[174:175], v[190:191], s[6:7], v[174:175] op_sel_hi:[1,0,1]
	v_cvt_pk_f32_fp8_e32 v[184:185], v122
	v_cvt_pk_f32_fp8_sdwa v[186:187], v122 src0_sel:WORD_1
	s_nop 0
	v_pk_fma_f32 v[176:177], v[184:185], s[6:7], v[176:177] op_sel_hi:[1,0,1]
	v_pk_fma_f32 v[178:179], v[186:187], s[6:7], v[178:179] op_sel_hi:[1,0,1]
	v_cvt_pk_f32_fp8_e32 v[188:189], v123
	v_cvt_pk_f32_fp8_sdwa v[190:191], v123 src0_sel:WORD_1
	s_nop 0
	v_pk_fma_f32 v[180:181], v[188:189], s[6:7], v[180:181] op_sel_hi:[1,0,1]
	v_pk_fma_f32 v[182:183], v[190:191], s[6:7], v[182:183] op_sel_hi:[1,0,1]

.Lcb_ov_done6:
	s_add_i32 s9, s8, 0x3000
	s_cmp_eq_u32 s52, 3
	s_cbranch_scc0 .Lcb_mid6
	s_lshl_b32 s10, s9, 12
	s_add_u32 s12, s14, s10
	s_addc_u32 s13, s15, 0
	global_store_dwordx4 v214, v[168:171], s[12:13]
	global_store_dwordx4 v214, v[172:175], s[12:13] offset:16
	global_store_dwordx4 v214, v[176:179], s[12:13] offset:32
	global_store_dwordx4 v214, v[180:183], s[12:13] offset:48
	s_branch .Lcb_done6

.Lcb_done6:
	s_add_i32 s9, s8, 0x6000
	s_lshr_b32 s10, s9, 12
	s_lshl_b32 s10, s10, 18
	s_and_b32 s12, s9, 0xfff
	s_lshl_b32 s12, s12, 2
	s_add_i32 s10, s10, s12
	s_add_u32 s12, s0, 0x37b00000
	s_addc_u32 s13, s1, 0
	s_add_u32 s12, s12, s10
	s_addc_u32 s13, s13, 0
	global_load_dword v66, v215, s[12:13]
	s_lshl_b32 s10, s9, 11
	s_add_u32 s12, s0, 0x37e00000
	s_addc_u32 s13, s1, 0
	s_add_u32 s12, s12, s10
	s_addc_u32 s13, s13, 0
	global_load_dwordx4 v[18:21], v213, s[12:13] nt
	global_load_dwordx4 v[22:25], v213, s[12:13] offset:16 nt
	s_waitcnt vmcnt(26)
	v_cmp_le_i32_e64 s[24:25], 0, v70
	s_mov_b32 s10, 0
	s_and_b32 s9, s24, 0xffff
	s_cmp_lg_u32 s9, 0
	s_cbranch_scc0 .Lcb_n10_0
	s_ff1_i32_b32 s26, s9
	s_add_i32 s27, s9, -1
	v_readlane_b32 s26, v70, s26
	s_and_b32 s9, s9, s27
	s_bitset1_b32 s10, 0
	s_lshl_b32 s26, s26, 10
	s_add_u32 s26, s4, s26
	s_addc_u32 s27, s5, 0
	s_branch .Lcb_l10_0

.Lcb_l10_0:
	global_load_dwordx4 v[120:123], v212, s[26:27] nt
	s_cmp_lg_u32 s9, 0
	s_cbranch_scc0 .Lcb_n10_1
	s_ff1_i32_b32 s26, s9
	s_add_i32 s27, s9, -1
	v_readlane_b32 s26, v70, s26
	s_and_b32 s9, s9, s27
	s_bitset1_b32 s10, 1
	s_lshl_b32 s26, s26, 10
	s_add_u32 s26, s4, s26
	s_addc_u32 s27, s5, 0
	s_branch .Lcb_l10_1

.Lcb_l10_1:
	global_load_dwordx4 v[124:127], v212, s[26:27] nt
	s_cmp_lg_u32 s9, 0
	s_cbranch_scc0 .Lcb_n10_2
	s_ff1_i32_b32 s26, s9
	s_add_i32 s27, s9, -1
	v_readlane_b32 s26, v70, s26
	s_and_b32 s9, s9, s27
	s_bitset1_b32 s10, 2
	s_lshl_b32 s26, s26, 10
	s_add_u32 s26, s4, s26
	s_addc_u32 s27, s5, 0
	s_branch .Lcb_l10_2

.Lcb_l10_2:
	global_load_dwordx4 v[128:131], v212, s[26:27] nt
	s_cmp_lg_u32 s9, 0
	s_cbranch_scc0 .Lcb_n10_3
	s_ff1_i32_b32 s26, s9
	s_add_i32 s27, s9, -1
	v_readlane_b32 s26, v70, s26
	s_and_b32 s9, s9, s27
	s_bitset1_b32 s10, 3
	s_lshl_b32 s26, s26, 10
	s_add_u32 s26, s4, s26
	s_addc_u32 s27, s5, 0
	s_branch .Lcb_l10_3

.Lcb_l10_3:
	global_load_dwordx4 v[132:135], v212, s[26:27] nt
	s_cmp_lg_u32 s9, 0
	s_cbranch_scc0 .Lcb_n10_4
	s_ff1_i32_b32 s26, s9
	s_add_i32 s27, s9, -1
	v_readlane_b32 s26, v70, s26
	s_and_b32 s9, s9, s27
	s_bitset1_b32 s10, 4
	s_lshl_b32 s26, s26, 10
	s_add_u32 s26, s4, s26
	s_addc_u32 s27, s5, 0
	s_branch .Lcb_l10_4

.Lcb_l10_4:
	global_load_dwordx4 v[136:139], v212, s[26:27] nt
	s_cmp_lg_u32 s9, 0
	s_cbranch_scc0 .Lcb_n10_5
	s_ff1_i32_b32 s26, s9
	s_add_i32 s27, s9, -1
	v_readlane_b32 s26, v70, s26
	s_and_b32 s9, s9, s27
	s_bitset1_b32 s10, 5
	s_lshl_b32 s26, s26, 10
	s_add_u32 s26, s4, s26
	s_addc_u32 s27, s5, 0
	s_branch .Lcb_l10_5

.Lcb_l10_5:
	global_load_dwordx4 v[140:143], v212, s[26:27] nt
	v_writelane_b32 v210, s10, 10
	v_writelane_b32 v211, s9, 10
	s_waitcnt vmcnt(39)
	v_lshlrev_b32_e32 v168, 16, v26
	v_and_b32_e32 v169, 0xffff0000, v26
	v_lshlrev_b32_e32 v170, 16, v27
	v_and_b32_e32 v171, 0xffff0000, v27
	v_lshlrev_b32_e32 v172, 16, v28
	v_and_b32_e32 v173, 0xffff0000, v28
	v_lshlrev_b32_e32 v174, 16, v29
	v_and_b32_e32 v175, 0xffff0000, v29
	v_lshlrev_b32_e32 v176, 16, v30
	v_and_b32_e32 v177, 0xffff0000, v30
	v_lshlrev_b32_e32 v178, 16, v31
	v_and_b32_e32 v179, 0xffff0000, v31
	v_lshlrev_b32_e32 v180, 16, v32
	v_and_b32_e32 v181, 0xffff0000, v32
	v_lshlrev_b32_e32 v182, 16, v33
	v_and_b32_e32 v183, 0xffff0000, v33
	v_readlane_b32 s10, v210, 7
	v_readlane_b32 s9, v211, 7
	s_bitcmp1_b32 s10, 0
	s_cbranch_scc0 .Lcb_s7_0
	v_cvt_pk_f32_fp8_e32 v[184:185], v144
	v_cvt_pk_f32_fp8_sdwa v[186:187], v144 src0_sel:WORD_1
	s_nop 0
	v_pk_fma_f32 v[168:169], v[184:185], s[6:7], v[168:169] op_sel_hi:[1,0,1]
	v_pk_fma_f32 v[170:171], v[186:187], s[6:7], v[170:171] op_sel_hi:[1,0,1]
	v_cvt_pk_f32_fp8_e32 v[188:189], v145
	v_cvt_pk_f32_fp8_sdwa v[190:191], v145 src0_sel:WORD_1
	s_nop 0
	v_pk_fma_f32 v[172:173], v[188:189], s[6:7], v[172:173] op_sel_hi:[1,0,1]
	v_pk_fma_f32 v[174:175], v[190:191], s[6:7], v[174:175] op_sel_hi:[1,0,1]
	v_cvt_pk_f32_fp8_e32 v[184:185], v146
	v_cvt_pk_f32_fp8_sdwa v[186:187], v146 src0_sel:WORD_1
	s_nop 0
	v_pk_fma_f32 v[176:177], v[184:185], s[6:7], v[176:177] op_sel_hi:[1,0,1]
	v_pk_fma_f32 v[178:179], v[186:187], s[6:7], v[178:179] op_sel_hi:[1,0,1]
	v_cvt_pk_f32_fp8_e32 v[188:189], v147
	v_cvt_pk_f32_fp8_sdwa v[190:191], v147 src0_sel:WORD_1
	s_nop 0
	v_pk_fma_f32 v[180:181], v[188:189], s[6:7], v[180:181] op_sel_hi:[1,0,1]
	v_pk_fma_f32 v[182:183], v[190:191], s[6:7], v[182:183] op_sel_hi:[1,0,1]

.Lcb_ov_done7:
	s_add_i32 s9, s8, 0x3800
	s_cmp_eq_u32 s52, 3
	s_cbranch_scc0 .Lcb_mid7
	s_lshl_b32 s10, s9, 12
	s_add_u32 s12, s14, s10
	s_addc_u32 s13, s15, 0
	global_store_dwordx4 v214, v[168:171], s[12:13]
	global_store_dwordx4 v214, v[172:175], s[12:13] offset:16
	global_store_dwordx4 v214, v[176:179], s[12:13] offset:32
	global_store_dwordx4 v214, v[180:183], s[12:13] offset:48
	s_branch .Lcb_done7

.Lcb_done7:
	s_add_i32 s9, s8, 0x6800
	s_lshr_b32 s10, s9, 12
	s_lshl_b32 s10, s10, 18
	s_and_b32 s12, s9, 0xfff
	s_lshl_b32 s12, s12, 2
	s_add_i32 s10, s10, s12
	s_add_u32 s12, s0, 0x37b00000
	s_addc_u32 s13, s1, 0
	s_add_u32 s12, s12, s10
	s_addc_u32 s13, s13, 0
	global_load_dword v67, v215, s[12:13]
	s_lshl_b32 s10, s9, 11
	s_add_u32 s12, s0, 0x37e00000
	s_addc_u32 s13, s1, 0
	s_add_u32 s12, s12, s10
	s_addc_u32 s13, s13, 0
	global_load_dwordx4 v[26:29], v213, s[12:13] nt
	global_load_dwordx4 v[30:33], v213, s[12:13] offset:16 nt
	s_waitcnt vmcnt(26)
	v_cmp_le_i32_e64 s[24:25], 0, v71
	s_mov_b32 s10, 0
	s_and_b32 s9, s24, 0xffff
	s_cmp_lg_u32 s9, 0
	s_cbranch_scc0 .Lcb_n11_0
	s_ff1_i32_b32 s26, s9
	s_add_i32 s27, s9, -1
	v_readlane_b32 s26, v71, s26
	s_and_b32 s9, s9, s27
	s_bitset1_b32 s10, 0
	s_lshl_b32 s26, s26, 10
	s_add_u32 s26, s4, s26
	s_addc_u32 s27, s5, 0
	s_branch .Lcb_l11_0

.Lcb_l11_0:
	global_load_dwordx4 v[144:147], v212, s[26:27] nt
	s_cmp_lg_u32 s9, 0
	s_cbranch_scc0 .Lcb_n11_1
	s_ff1_i32_b32 s26, s9
	s_add_i32 s27, s9, -1
	v_readlane_b32 s26, v71, s26
	s_and_b32 s9, s9, s27
	s_bitset1_b32 s10, 1
	s_lshl_b32 s26, s26, 10
	s_add_u32 s26, s4, s26
	s_addc_u32 s27, s5, 0
	s_branch .Lcb_l11_1

.Lcb_l11_1:
	global_load_dwordx4 v[148:151], v212, s[26:27] nt
	s_cmp_lg_u32 s9, 0
	s_cbranch_scc0 .Lcb_n11_2
	s_ff1_i32_b32 s26, s9
	s_add_i32 s27, s9, -1
	v_readlane_b32 s26, v71, s26
	s_and_b32 s9, s9, s27
	s_bitset1_b32 s10, 2
	s_lshl_b32 s26, s26, 10
	s_add_u32 s26, s4, s26
	s_addc_u32 s27, s5, 0
	s_branch .Lcb_l11_2

.Lcb_l11_2:
	global_load_dwordx4 v[152:155], v212, s[26:27] nt
	s_cmp_lg_u32 s9, 0
	s_cbranch_scc0 .Lcb_n11_3
	s_ff1_i32_b32 s26, s9
	s_add_i32 s27, s9, -1
	v_readlane_b32 s26, v71, s26
	s_and_b32 s9, s9, s27
	s_bitset1_b32 s10, 3
	s_lshl_b32 s26, s26, 10
	s_add_u32 s26, s4, s26
	s_addc_u32 s27, s5, 0
	s_branch .Lcb_l11_3

.Lcb_l11_3:
	global_load_dwordx4 v[156:159], v212, s[26:27] nt
	s_cmp_lg_u32 s9, 0
	s_cbranch_scc0 .Lcb_n11_4
	s_ff1_i32_b32 s26, s9
	s_add_i32 s27, s9, -1
	v_readlane_b32 s26, v71, s26
	s_and_b32 s9, s9, s27
	s_bitset1_b32 s10, 4
	s_lshl_b32 s26, s26, 10
	s_add_u32 s26, s4, s26
	s_addc_u32 s27, s5, 0
	s_branch .Lcb_l11_4

.Lcb_l11_4:
	global_load_dwordx4 v[160:163], v212, s[26:27] nt
	s_cmp_lg_u32 s9, 0
	s_cbranch_scc0 .Lcb_n11_5
	s_ff1_i32_b32 s26, s9
	s_add_i32 s27, s9, -1
	v_readlane_b32 s26, v71, s26
	s_and_b32 s9, s9, s27
	s_bitset1_b32 s10, 5
	s_lshl_b32 s26, s26, 10
	s_add_u32 s26, s4, s26
	s_addc_u32 s27, s5, 0
	s_branch .Lcb_l11_5

.Lcb_l11_5:
	global_load_dwordx4 v[164:167], v212, s[26:27] nt
	v_writelane_b32 v210, s10, 11
	v_writelane_b32 v211, s9, 11
	s_waitcnt vmcnt(39)
	v_lshlrev_b32_e32 v168, 16, v34
	v_and_b32_e32 v169, 0xffff0000, v34
	v_lshlrev_b32_e32 v170, 16, v35
	v_and_b32_e32 v171, 0xffff0000, v35
	v_lshlrev_b32_e32 v172, 16, v36
	v_and_b32_e32 v173, 0xffff0000, v36
	v_lshlrev_b32_e32 v174, 16, v37
	v_and_b32_e32 v175, 0xffff0000, v37
	v_lshlrev_b32_e32 v176, 16, v38
	v_and_b32_e32 v177, 0xffff0000, v38
	v_lshlrev_b32_e32 v178, 16, v39
	v_and_b32_e32 v179, 0xffff0000, v39
	v_lshlrev_b32_e32 v180, 16, v40
	v_and_b32_e32 v181, 0xffff0000, v40
	v_lshlrev_b32_e32 v182, 16, v41
	v_and_b32_e32 v183, 0xffff0000, v41
	v_readlane_b32 s10, v210, 8
	v_readlane_b32 s9, v211, 8
	s_bitcmp1_b32 s10, 0
	s_cbranch_scc0 .Lcb_s8_0
	v_cvt_pk_f32_fp8_e32 v[184:185], v72
	v_cvt_pk_f32_fp8_sdwa v[186:187], v72 src0_sel:WORD_1
	s_nop 0
	v_pk_fma_f32 v[168:169], v[184:185], s[6:7], v[168:169] op_sel_hi:[1,0,1]
	v_pk_fma_f32 v[170:171], v[186:187], s[6:7], v[170:171] op_sel_hi:[1,0,1]
	v_cvt_pk_f32_fp8_e32 v[188:189], v73
	v_cvt_pk_f32_fp8_sdwa v[190:191], v73 src0_sel:WORD_1
	s_nop 0
	v_pk_fma_f32 v[172:173], v[188:189], s[6:7], v[172:173] op_sel_hi:[1,0,1]
	v_pk_fma_f32 v[174:175], v[190:191], s[6:7], v[174:175] op_sel_hi:[1,0,1]
	v_cvt_pk_f32_fp8_e32 v[184:185], v74
	v_cvt_pk_f32_fp8_sdwa v[186:187], v74 src0_sel:WORD_1
	s_nop 0
	v_pk_fma_f32 v[176:177], v[184:185], s[6:7], v[176:177] op_sel_hi:[1,0,1]
	v_pk_fma_f32 v[178:179], v[186:187], s[6:7], v[178:179] op_sel_hi:[1,0,1]
	v_cvt_pk_f32_fp8_e32 v[188:189], v75
	v_cvt_pk_f32_fp8_sdwa v[190:191], v75 src0_sel:WORD_1
	s_nop 0
	v_pk_fma_f32 v[180:181], v[188:189], s[6:7], v[180:181] op_sel_hi:[1,0,1]
	v_pk_fma_f32 v[182:183], v[190:191], s[6:7], v[182:183] op_sel_hi:[1,0,1]

.Lcb_ov_done8:
	s_add_i32 s9, s8, 0x4000
	s_cmp_eq_u32 s52, 3
	s_cbranch_scc0 .Lcb_mid8
	s_lshl_b32 s10, s9, 12
	s_add_u32 s12, s14, s10
	s_addc_u32 s13, s15, 0
	global_store_dwordx4 v214, v[168:171], s[12:13]
	global_store_dwordx4 v214, v[172:175], s[12:13] offset:16
	global_store_dwordx4 v214, v[176:179], s[12:13] offset:32
	global_store_dwordx4 v214, v[180:183], s[12:13] offset:48
	s_branch .Lcb_done8

.Lcb_done8:
	s_add_i32 s9, s8, 0x7000
	s_lshr_b32 s10, s9, 12
	s_lshl_b32 s10, s10, 18
	s_and_b32 s12, s9, 0xfff
	s_lshl_b32 s12, s12, 2
	s_add_i32 s10, s10, s12
	s_add_u32 s12, s0, 0x37b00000
	s_addc_u32 s13, s1, 0
	s_add_u32 s12, s12, s10
	s_addc_u32 s13, s13, 0
	global_load_dword v68, v215, s[12:13]
	s_lshl_b32 s10, s9, 11
	s_add_u32 s12, s0, 0x37e00000
	s_addc_u32 s13, s1, 0
	s_add_u32 s12, s12, s10
	s_addc_u32 s13, s13, 0
	global_load_dwordx4 v[34:37], v213, s[12:13] nt
	global_load_dwordx4 v[38:41], v213, s[12:13] offset:16 nt
	s_waitcnt vmcnt(26)
	v_cmp_le_i32_e64 s[24:25], 0, v66
	s_mov_b32 s10, 0
	s_and_b32 s9, s24, 0xffff
	s_cmp_lg_u32 s9, 0
	s_cbranch_scc0 .Lcb_n12_0
	s_ff1_i32_b32 s26, s9
	s_add_i32 s27, s9, -1
	v_readlane_b32 s26, v66, s26
	s_and_b32 s9, s9, s27
	s_bitset1_b32 s10, 0
	s_lshl_b32 s26, s26, 10
	s_add_u32 s26, s4, s26
	s_addc_u32 s27, s5, 0
	s_branch .Lcb_l12_0

.Lcb_l12_5:
	global_load_dwordx4 v[92:95], v212, s[26:27] nt
	v_writelane_b32 v210, s10, 12
	v_writelane_b32 v211, s9, 12
	s_waitcnt vmcnt(39)
	v_lshlrev_b32_e32 v168, 16, v42
	v_and_b32_e32 v169, 0xffff0000, v42
	v_lshlrev_b32_e32 v170, 16, v43
	v_and_b32_e32 v171, 0xffff0000, v43
	v_lshlrev_b32_e32 v172, 16, v44
	v_and_b32_e32 v173, 0xffff0000, v44
	v_lshlrev_b32_e32 v174, 16, v45
	v_and_b32_e32 v175, 0xffff0000, v45
	v_lshlrev_b32_e32 v176, 16, v46
	v_and_b32_e32 v177, 0xffff0000, v46
	v_lshlrev_b32_e32 v178, 16, v47
	v_and_b32_e32 v179, 0xffff0000, v47
	v_lshlrev_b32_e32 v180, 16, v48
	v_and_b32_e32 v181, 0xffff0000, v48
	v_lshlrev_b32_e32 v182, 16, v49
	v_and_b32_e32 v183, 0xffff0000, v49
	v_readlane_b32 s10, v210, 9
	v_readlane_b32 s9, v211, 9
	s_bitcmp1_b32 s10, 0
	s_cbranch_scc0 .Lcb_s9_0
	v_cvt_pk_f32_fp8_e32 v[184:185], v96
	v_cvt_pk_f32_fp8_sdwa v[186:187], v96 src0_sel:WORD_1
	s_nop 0
	v_pk_fma_f32 v[168:169], v[184:185], s[6:7], v[168:169] op_sel_hi:[1,0,1]
	v_pk_fma_f32 v[170:171], v[186:187], s[6:7], v[170:171] op_sel_hi:[1,0,1]
	v_cvt_pk_f32_fp8_e32 v[188:189], v97
	v_cvt_pk_f32_fp8_sdwa v[190:191], v97 src0_sel:WORD_1
	s_nop 0
	v_pk_fma_f32 v[172:173], v[188:189], s[6:7], v[172:173] op_sel_hi:[1,0,1]
	v_pk_fma_f32 v[174:175], v[190:191], s[6:7], v[174:175] op_sel_hi:[1,0,1]
	v_cvt_pk_f32_fp8_e32 v[184:185], v98
	v_cvt_pk_f32_fp8_sdwa v[186:187], v98 src0_sel:WORD_1
	s_nop 0
	v_pk_fma_f32 v[176:177], v[184:185], s[6:7], v[176:177] op_sel_hi:[1,0,1]
	v_pk_fma_f32 v[178:179], v[186:187], s[6:7], v[178:179] op_sel_hi:[1,0,1]
	v_cvt_pk_f32_fp8_e32 v[188:189], v99
	v_cvt_pk_f32_fp8_sdwa v[190:191], v99 src0_sel:WORD_1
	s_nop 0
	v_pk_fma_f32 v[180:181], v[188:189], s[6:7], v[180:181] op_sel_hi:[1,0,1]
	v_pk_fma_f32 v[182:183], v[190:191], s[6:7], v[182:183] op_sel_hi:[1,0,1]

.Lcb_ov_done9:
	s_add_i32 s9, s8, 0x4800
	s_cmp_eq_u32 s52, 3
	s_cbranch_scc0 .Lcb_mid9
	s_lshl_b32 s10, s9, 12
	s_add_u32 s12, s14, s10
	s_addc_u32 s13, s15, 0
	global_store_dwordx4 v214, v[168:171], s[12:13]
	global_store_dwordx4 v214, v[172:175], s[12:13] offset:16
	global_store_dwordx4 v214, v[176:179], s[12:13] offset:32
	global_store_dwordx4 v214, v[180:183], s[12:13] offset:48
	s_branch .Lcb_done9

.Lcb_done9:
	s_add_i32 s9, s8, 0x7800
	s_lshr_b32 s10, s9, 12
	s_lshl_b32 s10, s10, 18
	s_and_b32 s12, s9, 0xfff
	s_lshl_b32 s12, s12, 2
	s_add_i32 s10, s10, s12
	s_add_u32 s12, s0, 0x37b00000
	s_addc_u32 s13, s1, 0
	s_add_u32 s12, s12, s10
	s_addc_u32 s13, s13, 0
	global_load_dword v69, v215, s[12:13]
	s_lshl_b32 s10, s9, 11
	s_add_u32 s12, s0, 0x37e00000
	s_addc_u32 s13, s1, 0
	s_add_u32 s12, s12, s10
	s_addc_u32 s13, s13, 0
	global_load_dwordx4 v[42:45], v213, s[12:13] nt
	global_load_dwordx4 v[46:49], v213, s[12:13] offset:16 nt
	s_waitcnt vmcnt(26)
	v_cmp_le_i32_e64 s[24:25], 0, v67
	s_mov_b32 s10, 0
	s_and_b32 s9, s24, 0xffff
	s_cmp_lg_u32 s9, 0
	s_cbranch_scc0 .Lcb_n13_0
	s_ff1_i32_b32 s26, s9
	s_add_i32 s27, s9, -1
	v_readlane_b32 s26, v67, s26
	s_and_b32 s9, s9, s27
	s_bitset1_b32 s10, 0
	s_lshl_b32 s26, s26, 10
	s_add_u32 s26, s4, s26
	s_addc_u32 s27, s5, 0
	s_branch .Lcb_l13_0

.Lcb_l13_5:
	global_load_dwordx4 v[116:119], v212, s[26:27] nt
	v_writelane_b32 v210, s10, 13
	v_writelane_b32 v211, s9, 13
	s_waitcnt vmcnt(39)
	v_lshlrev_b32_e32 v168, 16, v50
	v_and_b32_e32 v169, 0xffff0000, v50
	v_lshlrev_b32_e32 v170, 16, v51
	v_and_b32_e32 v171, 0xffff0000, v51
	v_lshlrev_b32_e32 v172, 16, v52
	v_and_b32_e32 v173, 0xffff0000, v52
	v_lshlrev_b32_e32 v174, 16, v53
	v_and_b32_e32 v175, 0xffff0000, v53
	v_lshlrev_b32_e32 v176, 16, v54
	v_and_b32_e32 v177, 0xffff0000, v54
	v_lshlrev_b32_e32 v178, 16, v55
	v_and_b32_e32 v179, 0xffff0000, v55
	v_lshlrev_b32_e32 v180, 16, v56
	v_and_b32_e32 v181, 0xffff0000, v56
	v_lshlrev_b32_e32 v182, 16, v57
	v_and_b32_e32 v183, 0xffff0000, v57
	v_readlane_b32 s10, v210, 10
	v_readlane_b32 s9, v211, 10
	s_bitcmp1_b32 s10, 0
	s_cbranch_scc0 .Lcb_s10_0
	v_cvt_pk_f32_fp8_e32 v[184:185], v120
	v_cvt_pk_f32_fp8_sdwa v[186:187], v120 src0_sel:WORD_1
	s_nop 0
	v_pk_fma_f32 v[168:169], v[184:185], s[6:7], v[168:169] op_sel_hi:[1,0,1]
	v_pk_fma_f32 v[170:171], v[186:187], s[6:7], v[170:171] op_sel_hi:[1,0,1]
	v_cvt_pk_f32_fp8_e32 v[188:189], v121
	v_cvt_pk_f32_fp8_sdwa v[190:191], v121 src0_sel:WORD_1
	s_nop 0
	v_pk_fma_f32 v[172:173], v[188:189], s[6:7], v[172:173] op_sel_hi:[1,0,1]
	v_pk_fma_f32 v[174:175], v[190:191], s[6:7], v[174:175] op_sel_hi:[1,0,1]
	v_cvt_pk_f32_fp8_e32 v[184:185], v122
	v_cvt_pk_f32_fp8_sdwa v[186:187], v122 src0_sel:WORD_1
	s_nop 0
	v_pk_fma_f32 v[176:177], v[184:185], s[6:7], v[176:177] op_sel_hi:[1,0,1]
	v_pk_fma_f32 v[178:179], v[186:187], s[6:7], v[178:179] op_sel_hi:[1,0,1]
	v_cvt_pk_f32_fp8_e32 v[188:189], v123
	v_cvt_pk_f32_fp8_sdwa v[190:191], v123 src0_sel:WORD_1
	s_nop 0
	v_pk_fma_f32 v[180:181], v[188:189], s[6:7], v[180:181] op_sel_hi:[1,0,1]
	v_pk_fma_f32 v[182:183], v[190:191], s[6:7], v[182:183] op_sel_hi:[1,0,1]

.Lcb_ov_done10:
	s_add_i32 s9, s8, 0x5000
	s_cmp_eq_u32 s52, 3
	s_cbranch_scc0 .Lcb_mid10
	s_lshl_b32 s10, s9, 12
	s_add_u32 s12, s14, s10
	s_addc_u32 s13, s15, 0
	global_store_dwordx4 v214, v[168:171], s[12:13]
	global_store_dwordx4 v214, v[172:175], s[12:13] offset:16
	global_store_dwordx4 v214, v[176:179], s[12:13] offset:32
	global_store_dwordx4 v214, v[180:183], s[12:13] offset:48
	s_branch .Lcb_done10

.Lcb_done10:
	s_waitcnt vmcnt(23)
	v_cmp_le_i32_e64 s[24:25], 0, v68
	s_mov_b32 s10, 0
	s_and_b32 s9, s24, 0xffff
	s_cmp_lg_u32 s9, 0
	s_cbranch_scc0 .Lcb_n14_0
	s_ff1_i32_b32 s26, s9
	s_add_i32 s27, s9, -1
	v_readlane_b32 s26, v68, s26
	s_and_b32 s9, s9, s27
	s_bitset1_b32 s10, 0
	s_lshl_b32 s26, s26, 10
	s_add_u32 s26, s4, s26
	s_addc_u32 s27, s5, 0
	s_branch .Lcb_l14_0

.Lcb_l14_5:
	global_load_dwordx4 v[140:143], v212, s[26:27] nt
	v_writelane_b32 v210, s10, 14
	v_writelane_b32 v211, s9, 14
	s_waitcnt vmcnt(36)
	v_lshlrev_b32_e32 v168, 16, v58
	v_and_b32_e32 v169, 0xffff0000, v58
	v_lshlrev_b32_e32 v170, 16, v59
	v_and_b32_e32 v171, 0xffff0000, v59
	v_lshlrev_b32_e32 v172, 16, v60
	v_and_b32_e32 v173, 0xffff0000, v60
	v_lshlrev_b32_e32 v174, 16, v61
	v_and_b32_e32 v175, 0xffff0000, v61
	v_lshlrev_b32_e32 v176, 16, v62
	v_and_b32_e32 v177, 0xffff0000, v62
	v_lshlrev_b32_e32 v178, 16, v63
	v_and_b32_e32 v179, 0xffff0000, v63
	v_lshlrev_b32_e32 v180, 16, v64
	v_and_b32_e32 v181, 0xffff0000, v64
	v_lshlrev_b32_e32 v182, 16, v65
	v_and_b32_e32 v183, 0xffff0000, v65
	v_readlane_b32 s10, v210, 11
	v_readlane_b32 s9, v211, 11
	s_bitcmp1_b32 s10, 0
	s_cbranch_scc0 .Lcb_s11_0
	v_cvt_pk_f32_fp8_e32 v[184:185], v144
	v_cvt_pk_f32_fp8_sdwa v[186:187], v144 src0_sel:WORD_1
	s_nop 0
	v_pk_fma_f32 v[168:169], v[184:185], s[6:7], v[168:169] op_sel_hi:[1,0,1]
	v_pk_fma_f32 v[170:171], v[186:187], s[6:7], v[170:171] op_sel_hi:[1,0,1]
	v_cvt_pk_f32_fp8_e32 v[188:189], v145
	v_cvt_pk_f32_fp8_sdwa v[190:191], v145 src0_sel:WORD_1
	s_nop 0
	v_pk_fma_f32 v[172:173], v[188:189], s[6:7], v[172:173] op_sel_hi:[1,0,1]
	v_pk_fma_f32 v[174:175], v[190:191], s[6:7], v[174:175] op_sel_hi:[1,0,1]
	v_cvt_pk_f32_fp8_e32 v[184:185], v146
	v_cvt_pk_f32_fp8_sdwa v[186:187], v146 src0_sel:WORD_1
	s_nop 0
	v_pk_fma_f32 v[176:177], v[184:185], s[6:7], v[176:177] op_sel_hi:[1,0,1]
	v_pk_fma_f32 v[178:179], v[186:187], s[6:7], v[178:179] op_sel_hi:[1,0,1]
	v_cvt_pk_f32_fp8_e32 v[188:189], v147
	v_cvt_pk_f32_fp8_sdwa v[190:191], v147 src0_sel:WORD_1
	s_nop 0
	v_pk_fma_f32 v[180:181], v[188:189], s[6:7], v[180:181] op_sel_hi:[1,0,1]
	v_pk_fma_f32 v[182:183], v[190:191], s[6:7], v[182:183] op_sel_hi:[1,0,1]

.Lcb_ov_done11:
	s_add_i32 s9, s8, 0x5800
	s_cmp_eq_u32 s52, 3
	s_cbranch_scc0 .Lcb_mid11
	s_lshl_b32 s10, s9, 12
	s_add_u32 s12, s14, s10
	s_addc_u32 s13, s15, 0
	global_store_dwordx4 v214, v[168:171], s[12:13]
	global_store_dwordx4 v214, v[172:175], s[12:13] offset:16
	global_store_dwordx4 v214, v[176:179], s[12:13] offset:32
	global_store_dwordx4 v214, v[180:183], s[12:13] offset:48
	s_branch .Lcb_done11

.Lcb_done11:
	s_waitcnt vmcnt(20)
	v_cmp_le_i32_e64 s[24:25], 0, v69
	s_mov_b32 s10, 0
	s_and_b32 s9, s24, 0xffff
	s_cmp_lg_u32 s9, 0
	s_cbranch_scc0 .Lcb_n15_0
	s_ff1_i32_b32 s26, s9
	s_add_i32 s27, s9, -1
	v_readlane_b32 s26, v69, s26
	s_and_b32 s9, s9, s27
	s_bitset1_b32 s10, 0
	s_lshl_b32 s26, s26, 10
	s_add_u32 s26, s4, s26
	s_addc_u32 s27, s5, 0
	s_branch .Lcb_l15_0

.Lcb_l15_5:
	global_load_dwordx4 v[164:167], v212, s[26:27] nt
	v_writelane_b32 v210, s10, 15
	v_writelane_b32 v211, s9, 15
	s_waitcnt vmcnt(33)
	v_lshlrev_b32_e32 v168, 16, v18
	v_and_b32_e32 v169, 0xffff0000, v18
	v_lshlrev_b32_e32 v170, 16, v19
	v_and_b32_e32 v171, 0xffff0000, v19
	v_lshlrev_b32_e32 v172, 16, v20
	v_and_b32_e32 v173, 0xffff0000, v20
	v_lshlrev_b32_e32 v174, 16, v21
	v_and_b32_e32 v175, 0xffff0000, v21
	v_lshlrev_b32_e32 v176, 16, v22
	v_and_b32_e32 v177, 0xffff0000, v22
	v_lshlrev_b32_e32 v178, 16, v23
	v_and_b32_e32 v179, 0xffff0000, v23
	v_lshlrev_b32_e32 v180, 16, v24
	v_and_b32_e32 v181, 0xffff0000, v24
	v_lshlrev_b32_e32 v182, 16, v25
	v_and_b32_e32 v183, 0xffff0000, v25
	v_readlane_b32 s10, v210, 12
	v_readlane_b32 s9, v211, 12
	s_bitcmp1_b32 s10, 0
	s_cbranch_scc0 .Lcb_s12_0
	v_cvt_pk_f32_fp8_e32 v[184:185], v72
	v_cvt_pk_f32_fp8_sdwa v[186:187], v72 src0_sel:WORD_1
	s_nop 0
	v_pk_fma_f32 v[168:169], v[184:185], s[6:7], v[168:169] op_sel_hi:[1,0,1]
	v_pk_fma_f32 v[170:171], v[186:187], s[6:7], v[170:171] op_sel_hi:[1,0,1]
	v_cvt_pk_f32_fp8_e32 v[188:189], v73
	v_cvt_pk_f32_fp8_sdwa v[190:191], v73 src0_sel:WORD_1
	s_nop 0
	v_pk_fma_f32 v[172:173], v[188:189], s[6:7], v[172:173] op_sel_hi:[1,0,1]
	v_pk_fma_f32 v[174:175], v[190:191], s[6:7], v[174:175] op_sel_hi:[1,0,1]
	v_cvt_pk_f32_fp8_e32 v[184:185], v74
	v_cvt_pk_f32_fp8_sdwa v[186:187], v74 src0_sel:WORD_1
	s_nop 0
	v_pk_fma_f32 v[176:177], v[184:185], s[6:7], v[176:177] op_sel_hi:[1,0,1]
	v_pk_fma_f32 v[178:179], v[186:187], s[6:7], v[178:179] op_sel_hi:[1,0,1]
	v_cvt_pk_f32_fp8_e32 v[188:189], v75
	v_cvt_pk_f32_fp8_sdwa v[190:191], v75 src0_sel:WORD_1
	s_nop 0
	v_pk_fma_f32 v[180:181], v[188:189], s[6:7], v[180:181] op_sel_hi:[1,0,1]
	v_pk_fma_f32 v[182:183], v[190:191], s[6:7], v[182:183] op_sel_hi:[1,0,1]

.Lcb_ov_done12:
	s_add_i32 s9, s8, 0x6000
	s_cmp_eq_u32 s52, 3
	s_cbranch_scc0 .Lcb_mid12
	s_lshl_b32 s10, s9, 12
	s_add_u32 s12, s14, s10
	s_addc_u32 s13, s15, 0
	global_store_dwordx4 v214, v[168:171], s[12:13]
	global_store_dwordx4 v214, v[172:175], s[12:13] offset:16
	global_store_dwordx4 v214, v[176:179], s[12:13] offset:32
	global_store_dwordx4 v214, v[180:183], s[12:13] offset:48
	s_branch .Lcb_done12

.Lcb_done12:
	s_waitcnt vmcnt(24)
	v_lshlrev_b32_e32 v168, 16, v26
	v_and_b32_e32 v169, 0xffff0000, v26
	v_lshlrev_b32_e32 v170, 16, v27
	v_and_b32_e32 v171, 0xffff0000, v27
	v_lshlrev_b32_e32 v172, 16, v28
	v_and_b32_e32 v173, 0xffff0000, v28
	v_lshlrev_b32_e32 v174, 16, v29
	v_and_b32_e32 v175, 0xffff0000, v29
	v_lshlrev_b32_e32 v176, 16, v30
	v_and_b32_e32 v177, 0xffff0000, v30
	v_lshlrev_b32_e32 v178, 16, v31
	v_and_b32_e32 v179, 0xffff0000, v31
	v_lshlrev_b32_e32 v180, 16, v32
	v_and_b32_e32 v181, 0xffff0000, v32
	v_lshlrev_b32_e32 v182, 16, v33
	v_and_b32_e32 v183, 0xffff0000, v33
	v_readlane_b32 s10, v210, 13
	v_readlane_b32 s9, v211, 13
	s_bitcmp1_b32 s10, 0
	s_cbranch_scc0 .Lcb_s13_0
	v_cvt_pk_f32_fp8_e32 v[184:185], v96
	v_cvt_pk_f32_fp8_sdwa v[186:187], v96 src0_sel:WORD_1
	s_nop 0
	v_pk_fma_f32 v[168:169], v[184:185], s[6:7], v[168:169] op_sel_hi:[1,0,1]
	v_pk_fma_f32 v[170:171], v[186:187], s[6:7], v[170:171] op_sel_hi:[1,0,1]
	v_cvt_pk_f32_fp8_e32 v[188:189], v97
	v_cvt_pk_f32_fp8_sdwa v[190:191], v97 src0_sel:WORD_1
	s_nop 0
	v_pk_fma_f32 v[172:173], v[188:189], s[6:7], v[172:173] op_sel_hi:[1,0,1]
	v_pk_fma_f32 v[174:175], v[190:191], s[6:7], v[174:175] op_sel_hi:[1,0,1]
	v_cvt_pk_f32_fp8_e32 v[184:185], v98
	v_cvt_pk_f32_fp8_sdwa v[186:187], v98 src0_sel:WORD_1
	s_nop 0
	v_pk_fma_f32 v[176:177], v[184:185], s[6:7], v[176:177] op_sel_hi:[1,0,1]
	v_pk_fma_f32 v[178:179], v[186:187], s[6:7], v[178:179] op_sel_hi:[1,0,1]
	v_cvt_pk_f32_fp8_e32 v[188:189], v99
	v_cvt_pk_f32_fp8_sdwa v[190:191], v99 src0_sel:WORD_1
	s_nop 0
	v_pk_fma_f32 v[180:181], v[188:189], s[6:7], v[180:181] op_sel_hi:[1,0,1]
	v_pk_fma_f32 v[182:183], v[190:191], s[6:7], v[182:183] op_sel_hi:[1,0,1]

.Lcb_ov_done13:
	s_add_i32 s9, s8, 0x6800
	s_cmp_eq_u32 s52, 3
	s_cbranch_scc0 .Lcb_mid13
	s_lshl_b32 s10, s9, 12
	s_add_u32 s12, s14, s10
	s_addc_u32 s13, s15, 0
	global_store_dwordx4 v214, v[168:171], s[12:13]
	global_store_dwordx4 v214, v[172:175], s[12:13] offset:16
	global_store_dwordx4 v214, v[176:179], s[12:13] offset:32
	global_store_dwordx4 v214, v[180:183], s[12:13] offset:48
	s_branch .Lcb_done13

.Lcb_done13:
	s_waitcnt vmcnt(18)
	v_lshlrev_b32_e32 v168, 16, v34
	v_and_b32_e32 v169, 0xffff0000, v34
	v_lshlrev_b32_e32 v170, 16, v35
	v_and_b32_e32 v171, 0xffff0000, v35
	v_lshlrev_b32_e32 v172, 16, v36
	v_and_b32_e32 v173, 0xffff0000, v36
	v_lshlrev_b32_e32 v174, 16, v37
	v_and_b32_e32 v175, 0xffff0000, v37
	v_lshlrev_b32_e32 v176, 16, v38
	v_and_b32_e32 v177, 0xffff0000, v38
	v_lshlrev_b32_e32 v178, 16, v39
	v_and_b32_e32 v179, 0xffff0000, v39
	v_lshlrev_b32_e32 v180, 16, v40
	v_and_b32_e32 v181, 0xffff0000, v40
	v_lshlrev_b32_e32 v182, 16, v41
	v_and_b32_e32 v183, 0xffff0000, v41
	v_readlane_b32 s10, v210, 14
	v_readlane_b32 s9, v211, 14
	s_bitcmp1_b32 s10, 0
	s_cbranch_scc0 .Lcb_s14_0
	v_cvt_pk_f32_fp8_e32 v[184:185], v120
	v_cvt_pk_f32_fp8_sdwa v[186:187], v120 src0_sel:WORD_1
	s_nop 0
	v_pk_fma_f32 v[168:169], v[184:185], s[6:7], v[168:169] op_sel_hi:[1,0,1]
	v_pk_fma_f32 v[170:171], v[186:187], s[6:7], v[170:171] op_sel_hi:[1,0,1]
	v_cvt_pk_f32_fp8_e32 v[188:189], v121
	v_cvt_pk_f32_fp8_sdwa v[190:191], v121 src0_sel:WORD_1
	s_nop 0
	v_pk_fma_f32 v[172:173], v[188:189], s[6:7], v[172:173] op_sel_hi:[1,0,1]
	v_pk_fma_f32 v[174:175], v[190:191], s[6:7], v[174:175] op_sel_hi:[1,0,1]
	v_cvt_pk_f32_fp8_e32 v[184:185], v122
	v_cvt_pk_f32_fp8_sdwa v[186:187], v122 src0_sel:WORD_1
	s_nop 0
	v_pk_fma_f32 v[176:177], v[184:185], s[6:7], v[176:177] op_sel_hi:[1,0,1]
	v_pk_fma_f32 v[178:179], v[186:187], s[6:7], v[178:179] op_sel_hi:[1,0,1]
	v_cvt_pk_f32_fp8_e32 v[188:189], v123
	v_cvt_pk_f32_fp8_sdwa v[190:191], v123 src0_sel:WORD_1
	s_nop 0
	v_pk_fma_f32 v[180:181], v[188:189], s[6:7], v[180:181] op_sel_hi:[1,0,1]
	v_pk_fma_f32 v[182:183], v[190:191], s[6:7], v[182:183] op_sel_hi:[1,0,1]

.Lcb_ov_done14:
	s_add_i32 s9, s8, 0x7000
	s_cmp_eq_u32 s52, 3
	s_cbranch_scc0 .Lcb_mid14
	s_lshl_b32 s10, s9, 12
	s_add_u32 s12, s14, s10
	s_addc_u32 s13, s15, 0
	global_store_dwordx4 v214, v[168:171], s[12:13]
	global_store_dwordx4 v214, v[172:175], s[12:13] offset:16
	global_store_dwordx4 v214, v[176:179], s[12:13] offset:32
	global_store_dwordx4 v214, v[180:183], s[12:13] offset:48
	s_branch .Lcb_done14

.Lcb_done14:
	s_waitcnt vmcnt(12)
	v_lshlrev_b32_e32 v168, 16, v42
	v_and_b32_e32 v169, 0xffff0000, v42
	v_lshlrev_b32_e32 v170, 16, v43
	v_and_b32_e32 v171, 0xffff0000, v43
	v_lshlrev_b32_e32 v172, 16, v44
	v_and_b32_e32 v173, 0xffff0000, v44
	v_lshlrev_b32_e32 v174, 16, v45
	v_and_b32_e32 v175, 0xffff0000, v45
	v_lshlrev_b32_e32 v176, 16, v46
	v_and_b32_e32 v177, 0xffff0000, v46
	v_lshlrev_b32_e32 v178, 16, v47
	v_and_b32_e32 v179, 0xffff0000, v47
	v_lshlrev_b32_e32 v180, 16, v48
	v_and_b32_e32 v181, 0xffff0000, v48
	v_lshlrev_b32_e32 v182, 16, v49
	v_and_b32_e32 v183, 0xffff0000, v49
	v_readlane_b32 s10, v210, 15
	v_readlane_b32 s9, v211, 15
	s_bitcmp1_b32 s10, 0
	s_cbranch_scc0 .Lcb_s15_0
	v_cvt_pk_f32_fp8_e32 v[184:185], v144
	v_cvt_pk_f32_fp8_sdwa v[186:187], v144 src0_sel:WORD_1
	s_nop 0
	v_pk_fma_f32 v[168:169], v[184:185], s[6:7], v[168:169] op_sel_hi:[1,0,1]
	v_pk_fma_f32 v[170:171], v[186:187], s[6:7], v[170:171] op_sel_hi:[1,0,1]
	v_cvt_pk_f32_fp8_e32 v[188:189], v145
	v_cvt_pk_f32_fp8_sdwa v[190:191], v145 src0_sel:WORD_1
	s_nop 0
	v_pk_fma_f32 v[172:173], v[188:189], s[6:7], v[172:173] op_sel_hi:[1,0,1]
	v_pk_fma_f32 v[174:175], v[190:191], s[6:7], v[174:175] op_sel_hi:[1,0,1]
	v_cvt_pk_f32_fp8_e32 v[184:185], v146
	v_cvt_pk_f32_fp8_sdwa v[186:187], v146 src0_sel:WORD_1
	s_nop 0
	v_pk_fma_f32 v[176:177], v[184:185], s[6:7], v[176:177] op_sel_hi:[1,0,1]
	v_pk_fma_f32 v[178:179], v[186:187], s[6:7], v[178:179] op_sel_hi:[1,0,1]
	v_cvt_pk_f32_fp8_e32 v[188:189], v147
	v_cvt_pk_f32_fp8_sdwa v[190:191], v147 src0_sel:WORD_1
	s_nop 0
	v_pk_fma_f32 v[180:181], v[188:189], s[6:7], v[180:181] op_sel_hi:[1,0,1]
	v_pk_fma_f32 v[182:183], v[190:191], s[6:7], v[182:183] op_sel_hi:[1,0,1]

.Lcb_ov_done15:
	s_add_i32 s9, s8, 0x7800
	s_cmp_eq_u32 s52, 3
	s_cbranch_scc0 .Lcb_mid15
	s_lshl_b32 s10, s9, 12
	s_add_u32 s12, s14, s10
	s_addc_u32 s13, s15, 0
	global_store_dwordx4 v214, v[168:171], s[12:13]
	global_store_dwordx4 v214, v[172:175], s[12:13] offset:16
	global_store_dwordx4 v214, v[176:179], s[12:13] offset:32
	global_store_dwordx4 v214, v[180:183], s[12:13] offset:48
	s_branch .Lcb_done15

.Lcb_done15:
	s_branch .LBB0_1469
.Lcb_old:
	v_readlane_b32 s6, v253, 0
	v_readlane_b32 s7, v253, 1
	v_mov_b32_e32 v2, v0
	s_load_dwordx2 s[8:9], s[6:7], 0xa0
	v_readfirstlane_b32 s0, v2
	v_and_b32_e32 v34, 63, v2
	v_lshlrev_b32_e32 v2, 14, v2
	v_lshlrev_b32_e32 v10, 3, v34
	s_waitcnt lgkmcnt(0)
	s_add_u32 s12, s8, 0x57e00000
	s_addc_u32 s13, s9, 0
	s_ashr_i32 s0, s0, 6
	s_add_u32 s14, s8, 0x37b00000
	s_addc_u32 s15, s9, 0
	s_add_u32 s16, s8, 0x37e00000
	s_addc_u32 s17, s9, 0
	s_add_i32 s0, s0, s89
	s_cmp_lt_i32 s0, 0x8000
	s_cselect_b64 s[4:5], -1, 0
	s_cmpk_gt_i32 s0, 0x7fff
	v_and_b32_e32 v206, 0x3c000, v2
	s_cbranch_scc1 .LBB0_1427
	s_ashr_i32 s24, s0, 12
	s_ashr_i32 s25, s24, 31
	s_and_b32 s1, s0, 0xfff
	s_lshl_b64 s[24:25], s[24:25], 18
	s_add_u32 s24, s14, s24
	s_addc_u32 s25, s15, s25
	s_lshl_b32 s10, s1, 2
	s_ashr_i32 s1, s0, 31
	v_lshl_add_u64 v[2:3], s[24:25], 0, v[206:207]
	s_lshl_b64 s[24:25], s[0:1], 11
	v_lshl_add_u64 v[2:3], v[2:3], 0, s[10:11]
	s_add_u32 s24, s16, s24
	s_addc_u32 s25, s17, s25
	global_load_dword v50, v[2:3], off
	global_load_dwordx2 v[8:9], v10, s[24:25] nt
	global_load_dwordx2 v[6:7], v10, s[24:25] offset:512 nt
	s_nop 0
	global_load_dwordx2 v[2:3], v10, s[24:25] offset:1024 nt
	global_load_dwordx2 v[4:5], v10, s[24:25] offset:1536 nt
	s_add_i32 s24, s0, s90
	s_cmpk_gt_i32 s24, 0x7fff
	s_cbranch_scc1 .LBB0_1428
	s_ashr_i32 s26, s24, 12
	s_ashr_i32 s27, s26, 31
	s_and_b32 s1, s24, 0xfff
	s_lshl_b64 s[26:27], s[26:27], 18
	s_add_u32 s26, s14, s26
	s_addc_u32 s27, s15, s27
	s_ashr_i32 s25, s24, 31
	v_lshl_add_u64 v[12:13], s[26:27], 0, v[206:207]
	s_lshl_b32 s10, s1, 2
	s_lshl_b64 s[24:25], s[24:25], 11
	v_lshl_add_u64 v[12:13], v[12:13], 0, s[10:11]
	s_add_u32 s24, s16, s24
	s_addc_u32 s25, s17, s25
	global_load_dword v51, v[12:13], off
	global_load_dwordx2 v[18:19], v10, s[24:25] nt
	global_load_dwordx2 v[20:21], v10, s[24:25] offset:512 nt
	global_load_dwordx2 v[22:23], v10, s[24:25] offset:1024 nt
	global_load_dwordx2 v[24:25], v10, s[24:25] offset:1536 nt
	s_branch .LBB0_1429
